# conversion loops: first-half wait no longer covers the previous emit's stores (vmcnt 24 after first trip); on top of v36
# baseline (speedup 1.0000x reference)
; #define GAS __attribute__((address_space(1)))
; #define LAS __attribute__((address_space(3)))
; __device__ __forceinline__ void conv_load(const ConvSrc& c, int lane, f32x4 (&ra)[8], f32x4 (&rb)[8]) {
;     const int nblk = c.N >> 6, kb = c.kfast ? (c.item & 31) : c.item / nblk, nb = c.kfast ? (c.item >> 5) : c.item - kb * nblk, k0 = kb * 64, n0 = nb * 64;
;     const int n4 = (lane & 15) * 4, kq = lane >> 4;
; #pragma unroll
;     for (int i = 0; i < 8; ++i) { const int kp2 = 4 * i + kq; const float* p = c.W + (size_t)(k0 + 2 * kp2) * c.N + n0 + n4; ra[i] = __builtin_nontemporal_load((const GAS f32x4*)p); rb[i] = __builtin_nontemporal_load((const GAS f32x4*)(p + c.N)); }
; __device__ __forceinline__ void conv_run(KP kp, unsigned char* ws, LAS unsigned* P, int lane, int first, int it_hi, int step) {
;     if (first >= it_hi) return;
;     const int lastv = first + ((it_hi - 1 - first) / step) * step;
;     f32x4 a0[8], b0[8], a1[8], b1[8];
;     ConvSrc c0 = conv_decode(kp, ws, first), c1;
;     conv_load(c0, lane, a0, b0);
.LBB0_29:
	s_mul_i32 s14, s14, s5
	s_sub_i32 s11, s11, s14
	s_sub_i32 s14, s11, s5
	s_cmp_ge_u32 s11, s5
	s_cselect_b32 s11, s14, s11
	s_sub_i32 s14, s11, s5
	s_cmp_ge_u32 s11, s5
	s_cselect_b32 s5, s14, s11
	s_xor_b32 s5, s5, s10
	s_sub_i32 s5, s10, s5
	s_add_i32 s24, s2, s5
	s_mul_i32 s2, s82, 0x1500
	s_add_i32 s24, s24, s22
	s_add_i32 s4, s4, s2
	s_lshl_b32 s25, s16, 4
	s_add_u32 s6, s12, s6
	s_addc_u32 s7, s13, s7
	s_waitcnt lgkmcnt(0)
	s_add_u32 s14, s26, s8
	s_addc_u32 s15, s27, s9
	s_lshr_b32 s2, s21, 6
	v_cvt_f32_u32_e32 v0, s2
	s_sub_i32 s9, 0, s2
	s_abs_i32 s8, s17
	s_ashr_i32 s5, s17, 31
	v_rcp_iflag_f32_e32 v0, v0
	v_ashrrev_i32_e32 v132, 3, v64
	v_and_b32_e32 v133, -2, v132
	s_load_dwordx2 s[6:7], s[6:7], 0x0
	v_mul_f32_e32 v0, 0x4f7ffffe, v0
	v_cvt_u32_f32_e32 v0, v0
	v_and_b32_e32 v66, 60, v12
	v_mov_b32_e32 v129, 0
	v_lshlrev_b32_e32 v128, 2, v66
	v_readfirstlane_b32 s10, v0
	s_mul_i32 s9, s9, s10
	s_mul_hi_u32 s9, s10, s9
	s_add_i32 s10, s10, s9
	s_mul_hi_u32 s9, s8, s10
	s_mul_i32 s10, s9, s2
	s_sub_i32 s8, s8, s10
	s_add_i32 s10, s9, 1
	s_sub_i32 s11, s8, s2
	s_cmp_ge_u32 s8, s2
	s_cselect_b32 s9, s10, s9
	s_cselect_b32 s8, s11, s8
	s_add_i32 s10, s9, 1
	s_cmp_ge_u32 s8, s2
	s_cselect_b32 s8, s10, s9
	s_xor_b32 s8, s8, s5
	s_sub_i32 s5, s8, s5
	v_lshl_add_u32 v24, s5, 6, v133
	v_add_u32_e32 v0, 56, v24
	s_mul_i32 s5, s5, s2
	v_mad_i64_i32 v[0:1], s[8:9], v0, s21, 0
	s_sub_i32 s2, s17, s5
	s_lshl_b32 s8, s2, 6
	s_ashr_i32 s9, s8, 31
	s_waitcnt lgkmcnt(0)
	v_lshl_add_u64 v[0:1], v[0:1], 2, s[6:7]
	s_lshl_b64 s[8:9], s[8:9], 2
	v_lshl_add_u64 v[0:1], v[0:1], 0, s[8:9]
	v_add_u32_e32 v8, 16, v24
	v_add_u32_e32 v16, 32, v24
	v_lshl_add_u64 v[32:33], v[0:1], 0, v[128:129]
	v_mad_i64_i32 v[0:1], s[10:11], v24, s21, 0
	v_mad_i64_i32 v[8:9], s[10:11], v8, s21, 0
	v_mad_i64_i32 v[16:17], s[10:11], v16, s21, 0
	v_lshl_add_u64 v[0:1], v[0:1], 2, s[6:7]
	v_lshl_add_u64 v[8:9], v[8:9], 2, s[6:7]
	v_lshl_add_u64 v[16:17], v[16:17], 2, s[6:7]
	v_lshl_add_u64 v[0:1], v[0:1], 0, s[8:9]
	v_lshl_add_u64 v[8:9], v[8:9], 0, s[8:9]
	v_lshl_add_u64 v[16:17], v[16:17], 0, s[8:9]
	v_lshl_add_u64 v[36:37], v[0:1], 0, v[128:129]
	v_add_u32_e32 v0, 8, v24
	v_lshl_add_u64 v[40:41], v[8:9], 0, v[128:129]
	v_add_u32_e32 v8, 24, v24
	v_lshl_add_u64 v[44:45], v[16:17], 0, v[128:129]
	v_add_u32_e32 v16, 40, v24
	v_add_u32_e32 v24, 48, v24
	v_mad_i64_i32 v[0:1], s[10:11], v0, s21, 0
	v_mad_i64_i32 v[8:9], s[10:11], v8, s21, 0
	v_mad_i64_i32 v[16:17], s[10:11], v16, s21, 0
	v_mad_i64_i32 v[24:25], s[10:11], v24, s21, 0
	v_lshl_add_u64 v[0:1], v[0:1], 2, s[6:7]
	v_lshl_add_u64 v[8:9], v[8:9], 2, s[6:7]
	v_lshl_add_u64 v[16:17], v[16:17], 2, s[6:7]
	v_lshl_add_u64 v[24:25], v[24:25], 2, s[6:7]
	s_lshl_b32 s2, s21, 2
	v_lshl_add_u64 v[0:1], v[0:1], 0, s[8:9]
	v_lshl_add_u64 v[8:9], v[8:9], 0, s[8:9]
	v_lshl_add_u64 v[16:17], v[16:17], 0, s[8:9]
	v_lshl_add_u64 v[24:25], v[24:25], 0, s[8:9]
	v_lshl_add_u64 v[34:35], v[32:33], 0, s[2:3]
	v_lshl_add_u64 v[38:39], v[0:1], 0, v[128:129]
	v_lshl_add_u64 v[42:43], v[8:9], 0, v[128:129]
	v_lshl_add_u64 v[46:47], v[16:17], 0, v[128:129]
	v_lshl_add_u64 v[68:69], v[24:25], 0, v[128:129]
	global_load_dwordx4 v[0:3], v[36:37], off nt
	global_load_dwordx4 v[4:7], v[38:39], off nt
	global_load_dwordx4 v[8:11], v[40:41], off nt
	global_load_dwordx4 v[12:15], v[42:43], off nt
	global_load_dwordx4 v[16:19], v[44:45], off nt
	global_load_dwordx4 v[20:23], v[46:47], off nt
	global_load_dwordx4 v[24:27], v[34:35], off nt
	global_load_dwordx4 v[28:31], v[32:33], off nt
	v_lshl_add_u64 v[70:71], v[46:47], 0, s[2:3]
	v_lshl_add_u64 v[72:73], v[44:45], 0, s[2:3]
	v_lshl_add_u64 v[74:75], v[42:43], 0, s[2:3]
	v_lshl_add_u64 v[76:77], v[40:41], 0, s[2:3]
	v_lshl_add_u64 v[78:79], v[38:39], 0, s[2:3]
	v_lshl_add_u64 v[80:81], v[36:37], 0, s[2:3]
	v_lshl_add_u64 v[82:83], v[68:69], 0, s[2:3]
	global_load_dwordx4 v[36:39], v[68:69], off nt
	global_load_dwordx4 v[40:43], v[82:83], off nt
	global_load_dwordx4 v[60:63], v[70:71], off nt
	global_load_dwordx4 v[56:59], v[72:73], off nt
	global_load_dwordx4 v[52:55], v[74:75], off nt
	global_load_dwordx4 v[48:51], v[76:77], off nt
	global_load_dwordx4 v[44:47], v[78:79], off nt
	global_load_dwordx4 v[32:35], v[80:81], off nt
	s_add_u32 s18, s26, 0x26000000
	s_addc_u32 s19, s27, 0
	s_add_u32 s38, s26, 0x6000000
	s_addc_u32 s39, s27, 0
	s_add_u32 s6, s26, 0x5800000
	s_addc_u32 s7, s27, 0
	s_add_u32 s8, s26, 0x4800000
	s_addc_u32 s9, s27, 0
	v_ashrrev_i32_e32 v65, 4, v64
	s_movk_i32 s2, 0x104
	v_and_b32_e32 v64, 7, v64
	s_add_u32 s10, s26, 0x800000
	v_add_u32_e32 v67, s4, v128
	v_mul_lo_u32 v65, v65, s2
	v_mul_u32_u24_e32 v68, 0x410, v64
	v_lshlrev_b32_e32 v64, 3, v64
	v_lshlrev_b32_e32 v69, 2, v132
	s_addc_u32 s11, s27, 0
	v_add3_u32 v134, s4, v68, v69
	v_add_u32_e32 v135, 8, v132
	v_add_u32_e32 v136, 16, v132
	v_add_u32_e32 v137, 24, v132
	v_lshlrev_b32_e32 v128, 2, v66
	v_add_u32_e32 v138, 32, v132
	v_add_u32_e32 v139, 40, v132
	v_add_u32_e32 v140, v67, v65
	v_add_u32_e32 v141, 48, v132
	v_lshlrev_b32_e32 v130, 1, v64
	v_add_u32_e32 v142, 56, v132
	s_mov_b32 s98, 0
	s_branch .LBB0_31

; #define GAS __attribute__((address_space(1)))
; __device__ __forceinline__ void conv_load(const ConvSrc& c, int lane, f32x4 (&ra)[8], f32x4 (&rb)[8]) {
;     const int nblk = c.N >> 6, kb = c.kfast ? (c.item & 31) : c.item / nblk, nb = c.kfast ? (c.item >> 5) : c.item - kb * nblk, k0 = kb * 64, n0 = nb * 64;
;     const int n4 = (lane & 15) * 4, kq = lane >> 4;
; #pragma unroll
;     for (int i = 0; i < 8; ++i) { const int kp2 = 4 * i + kq; const float* p = c.W + (size_t)(k0 + 2 * kp2) * c.N + n0 + n4; ra[i] = __builtin_nontemporal_load((const GAS f32x4*)p); rb[i] = __builtin_nontemporal_load((const GAS f32x4*)(p + c.N)); }
; }
; __device__ __forceinline__ void conv_run(KP kp, unsigned char* ws, LAS unsigned* P, int lane, int first, int it_hi, int step) {
;     ...
;         c1 = conv_decode(kp, ws, min(it + step, lastv)); conv_load(c1, lane, a1, b1);
;         conv_emit(c0, lane, P, a0, b0);
.LBB0_50:
	s_lshr_b32 s34, s2, 6
	v_cvt_f32_u32_e32 v64, s34
	s_sub_i32 s29, 0, s34
	s_abs_i32 s28, s4
	s_ashr_i32 s20, s4, 31
	v_rcp_iflag_f32_e32 v64, v64
	v_mov_b32_e32 v131, v129
	v_mul_f32_e32 v64, 0x4f7ffffe, v64
	v_cvt_u32_f32_e32 v64, v64
	s_nop 0
	v_readfirstlane_b32 s35, v64
	s_mul_i32 s29, s29, s35
	s_mul_hi_u32 s29, s35, s29
	s_add_i32 s35, s35, s29
	s_mul_hi_u32 s29, s28, s35
	s_mul_i32 s35, s29, s34
	s_sub_i32 s28, s28, s35
	s_add_i32 s36, s29, 1
	s_sub_i32 s35, s28, s34
	s_cmp_ge_u32 s28, s34
	s_cselect_b32 s29, s36, s29
	s_cselect_b32 s28, s35, s28
	s_add_i32 s35, s29, 1
	s_cmp_ge_u32 s28, s34
	s_cselect_b32 s28, s35, s29
	s_xor_b32 s28, s28, s20
	s_sub_i32 s20, s28, s20
	v_lshl_add_u32 v80, s20, 6, v133
	v_mad_u64_u32 v[64:65], s[28:29], v80, s2, 0
	v_ashrrev_i32_e32 v67, 31, v80
	v_mov_b32_e32 v66, v65
	v_add_u32_e32 v68, 8, v80
	v_mad_u64_u32 v[66:67], s[28:29], v67, s2, v[66:67]
	v_mov_b32_e32 v65, v66
	v_mad_u64_u32 v[66:67], s[28:29], v68, s2, 0
	v_ashrrev_i32_e32 v69, 31, v68
	v_mov_b32_e32 v68, v67
	v_mad_u64_u32 v[68:69], s[28:29], v69, s2, v[68:69]
	v_mov_b32_e32 v67, v68
	v_add_u32_e32 v68, 16, v80
	v_ashrrev_i32_e32 v71, 31, v68
	v_mad_u64_u32 v[68:69], s[28:29], v68, s2, 0
	v_mov_b32_e32 v70, v69
	v_mad_u64_u32 v[70:71], s[28:29], v71, s2, v[70:71]
	v_mov_b32_e32 v69, v70
	v_add_u32_e32 v70, 24, v80
	v_ashrrev_i32_e32 v73, 31, v70
	v_mad_u64_u32 v[70:71], s[28:29], v70, s2, 0
	v_mov_b32_e32 v72, v71
	v_mad_u64_u32 v[72:73], s[28:29], v73, s2, v[72:73]
	v_mov_b32_e32 v71, v72
	v_add_u32_e32 v72, 32, v80
	v_ashrrev_i32_e32 v75, 31, v72
	v_mad_u64_u32 v[72:73], s[28:29], v72, s2, 0
	v_mov_b32_e32 v74, v73
	v_mad_u64_u32 v[74:75], s[28:29], v75, s2, v[74:75]
	v_mov_b32_e32 v73, v74
	v_add_u32_e32 v74, 40, v80
	v_ashrrev_i32_e32 v77, 31, v74
	v_mad_u64_u32 v[74:75], s[28:29], v74, s2, 0
	v_mov_b32_e32 v76, v75
	v_mad_u64_u32 v[76:77], s[28:29], v77, s2, v[76:77]
	v_mov_b32_e32 v75, v76
	v_add_u32_e32 v76, 48, v80
	v_ashrrev_i32_e32 v79, 31, v76
	v_mad_u64_u32 v[76:77], s[28:29], v76, s2, 0
	v_mov_b32_e32 v78, v77
	v_mad_u64_u32 v[78:79], s[28:29], v79, s2, v[78:79]
	v_mov_b32_e32 v77, v78
	v_add_u32_e32 v78, 56, v80
	v_ashrrev_i32_e32 v81, 31, v78
	v_mad_u64_u32 v[78:79], s[28:29], v78, s2, 0
	v_mov_b32_e32 v80, v79
	v_mad_u64_u32 v[80:81], s[28:29], v81, s2, v[80:81]
	s_mul_i32 s28, s20, s34
	s_sub_i32 s43, s4, s28
	s_lshl_b32 s28, s43, 6
	s_ashr_i32 s29, s28, 31
	v_mov_b32_e32 v79, v80
	s_waitcnt lgkmcnt(0)
	v_lshl_add_u64 v[64:65], v[64:65], 2, s[30:31]
	s_lshl_b64 s[34:35], s[28:29], 2
	v_lshl_add_u64 v[66:67], v[66:67], 2, s[30:31]
	v_lshl_add_u64 v[64:65], v[64:65], 0, s[34:35]
	v_lshl_add_u64 v[66:67], v[66:67], 0, s[34:35]
	v_lshl_add_u64 v[68:69], v[68:69], 2, s[30:31]
	v_lshl_add_u64 v[78:79], v[78:79], 2, s[30:31]
	v_lshl_add_u64 v[64:65], v[64:65], 0, v[128:129]
	s_lshl_b64 s[36:37], s[2:3], 2
	v_lshl_add_u64 v[66:67], v[66:67], 0, v[128:129]
	v_lshl_add_u64 v[68:69], v[68:69], 0, s[34:35]
	v_lshl_add_u64 v[70:71], v[70:71], 2, s[30:31]
	v_lshl_add_u64 v[78:79], v[78:79], 0, s[34:35]
	v_lshl_add_u64 v[68:69], v[68:69], 0, v[128:129]
	v_lshl_add_u64 v[70:71], v[70:71], 0, s[34:35]
	v_lshl_add_u64 v[72:73], v[72:73], 2, s[30:31]
	v_lshl_add_u64 v[144:145], v[78:79], 0, v[128:129]
	v_lshl_add_u64 v[78:79], v[64:65], 0, s[36:37]
	global_load_dwordx4 v[120:123], v[64:65], off nt
	global_load_dwordx4 v[124:127], v[78:79], off nt
	v_lshl_add_u64 v[64:65], v[66:67], 0, s[36:37]
	v_lshl_add_u64 v[70:71], v[70:71], 0, v[128:129]
	v_lshl_add_u64 v[72:73], v[72:73], 0, s[34:35]
	v_lshl_add_u64 v[74:75], v[74:75], 2, s[30:31]
	global_load_dwordx4 v[112:115], v[66:67], off nt
	global_load_dwordx4 v[116:119], v[64:65], off nt
	v_lshl_add_u64 v[64:65], v[68:69], 0, s[36:37]
	v_lshl_add_u64 v[72:73], v[72:73], 0, v[128:129]
	v_lshl_add_u64 v[74:75], v[74:75], 0, s[34:35]
	v_lshl_add_u64 v[76:77], v[76:77], 2, s[30:31]
	global_load_dwordx4 v[104:107], v[68:69], off nt
	global_load_dwordx4 v[108:111], v[64:65], off nt
	v_lshl_add_u64 v[64:65], v[70:71], 0, s[36:37]
	v_lshl_add_u64 v[74:75], v[74:75], 0, v[128:129]
	v_lshl_add_u64 v[76:77], v[76:77], 0, s[34:35]
	global_load_dwordx4 v[96:99], v[70:71], off nt
	global_load_dwordx4 v[100:103], v[64:65], off nt
	v_lshl_add_u64 v[64:65], v[72:73], 0, s[36:37]
	v_lshl_add_u64 v[76:77], v[76:77], 0, v[128:129]
	global_load_dwordx4 v[88:91], v[72:73], off nt
	global_load_dwordx4 v[92:95], v[64:65], off nt
	v_lshl_add_u64 v[64:65], v[74:75], 0, s[36:37]
	global_load_dwordx4 v[80:83], v[74:75], off nt
	global_load_dwordx4 v[84:87], v[64:65], off nt
	v_lshl_add_u64 v[64:65], v[76:77], 0, s[36:37]
	v_lshl_add_u64 v[68:69], v[144:145], 0, s[36:37]
	global_load_dwordx4 v[72:75], v[76:77], off nt
	s_nop 0
	global_load_dwordx4 v[76:79], v[64:65], off nt
	s_nop 0
	global_load_dwordx4 v[64:67], v[144:145], off nt
	s_nop 0
	global_load_dwordx4 v[68:71], v[68:69], off nt
	s_cmp_eq_u32 s98, 0
	s_cbranch_scc1 .Lcw_first_1
	s_waitcnt vmcnt(24)
	s_branch .Lcw_done_1
.Lcw_first_1:
	s_waitcnt vmcnt(16)
	s_mov_b32 s98, 1
; #define GAS __attribute__((address_space(1)))
; #define LAS __attribute__((address_space(3)))
; __device__ __forceinline__ ConvSrc conv_decode(KP kp, unsigned char* ws, int it) {
;     constexpr int I_IN = 32 * 256, I_SQ = 32 * 32, I_UP = 32 * 64, I_DN = 32 * 32;
;     ConvSrc c; int r = it; c.ldk = 2048; c.kfast = 0; c.tiled = 32; c.ktoff = 0;
;     if (r < I_IN) { c.W = (const float*)KIN(6); c.WT = (bf16*)(ws + WS_WIN); c.N = 16384; c.item = r; return c; } r -= I_IN;
;     if (r < I_SQ) { c.W = (const float*)KIN(13); c.WT = (bf16*)(ws + WS_WAO); c.N = 2048; c.item = r; c.ldk = 4096; c.tiled = 64; return c; } r -= I_SQ;
;     if (r < I_SQ) { c.W = (const float*)KIN(14); c.WT = (bf16*)(ws + WS_WAO); c.N = 2048; c.item = r; c.ldk = 4096; c.tiled = 64; c.ktoff = 32; return c; } r -= I_SQ;
;     if (r < I_SQ) { c.W = (const float*)KIN(15); c.WT = (bf16*)(ws + WS_WO); c.N = 2048; c.item = r; return c; } r -= I_SQ;
;     if (r < NE * I_UP) { const int e = r / I_UP; c.W = (const float*)KIN(19) + (size_t)e * 2048 * 4096; c.WT = (bf16*)(ws + WS_WUP) + (size_t)e * 4096 * 2048; c.N = 4096; c.item = r - e * I_UP; return c; } r -= NE * I_UP;
; __device__ __forceinline__ void conv_emit(const ConvSrc& c, int lane, LAS unsigned* P, const f32x4 (&ra)[8], const f32x4 (&rb)[8]) {
;     const int nblk = c.N >> 6, kb = c.kfast ? (c.item & 31) : c.item / nblk, nb = c.kfast ? (c.item >> 5) : c.item - kb * nblk, k0 = kb * 64, n0 = nb * 64;
;     const int n4 = (lane & 15) * 4, kq = lane >> 4;
; #pragma unroll
;     for (int i = 0; i < 8; ++i) { const int kp2 = 4 * i + kq; LAS unsigned* d = P + kp2 * 65 + n4;
;         d[0] = pg8::cvt_pk_bf16(ra[i].x, rb[i].x); d[1] = pg8::cvt_pk_bf16(ra[i].y, rb[i].y); d[2] = pg8::cvt_pk_bf16(ra[i].z, rb[i].z); d[3] = pg8::cvt_pk_bf16(ra[i].w, rb[i].w); }
;     LDS_WAIT(); asm volatile("" ::: "memory");
;     const int cc = lane & 7;
; #pragma unroll
;     for (int jj = 0; jj < 8; ++jj) { const int n = (lane >> 3) + 8 * jj; const LAS unsigned* sp = P + (4 * cc) * 65 + n;
;         v4u o; o.x = sp[0]; o.y = sp[65]; o.z = sp[130]; o.w = sp[195];
;         bf16* dst = c.tiled ? c.WT + (size_t)((nb >> 2) * c.tiled + c.ktoff + kb) * 16384 + ((nb & 3) * 64 + n) * 64 + 8 * cc : c.WT + (size_t)(n0 + n) * c.ldk + k0 + 8 * cc;
;         __builtin_nontemporal_store(o, (GAS v4u*)dst); }
;     LDS_WAIT(); asm volatile("" ::: "memory");
.Lcw_done_1:
	v_cvt_pk_bf16_f32 v0, v0, v32
	ds_write_b32 v140, v0
	v_cvt_pk_bf16_f32 v0, v1, v33
	ds_write_b32 v140, v0 offset:4
	v_cvt_pk_bf16_f32 v0, v2, v34
	ds_write_b32 v140, v0 offset:8
	v_cvt_pk_bf16_f32 v0, v3, v35
	ds_write_b32 v140, v0 offset:12
	v_cvt_pk_bf16_f32 v0, v4, v44
	ds_write_b32 v140, v0 offset:1040
	v_cvt_pk_bf16_f32 v0, v5, v45
	ds_write_b32 v140, v0 offset:1044
	v_cvt_pk_bf16_f32 v0, v6, v46
	ds_write_b32 v140, v0 offset:1048
	v_cvt_pk_bf16_f32 v0, v7, v47
	ds_write_b32 v140, v0 offset:1052
	v_cvt_pk_bf16_f32 v0, v8, v48
	ds_write_b32 v140, v0 offset:2080
	v_cvt_pk_bf16_f32 v0, v9, v49
	ds_write_b32 v140, v0 offset:2084
	v_cvt_pk_bf16_f32 v0, v10, v50
	ds_write_b32 v140, v0 offset:2088
	v_cvt_pk_bf16_f32 v0, v11, v51
	ds_write_b32 v140, v0 offset:2092
	v_cvt_pk_bf16_f32 v0, v12, v52
	ds_write_b32 v140, v0 offset:3120
	v_cvt_pk_bf16_f32 v0, v13, v53
	ds_write_b32 v140, v0 offset:3124
	v_cvt_pk_bf16_f32 v0, v14, v54
	ds_write_b32 v140, v0 offset:3128
	v_cvt_pk_bf16_f32 v0, v15, v55
	ds_write_b32 v140, v0 offset:3132
	v_cvt_pk_bf16_f32 v0, v16, v56
	ds_write_b32 v140, v0 offset:4160
	v_cvt_pk_bf16_f32 v0, v17, v57
	ds_write_b32 v140, v0 offset:4164
	v_cvt_pk_bf16_f32 v0, v18, v58
	ds_write_b32 v140, v0 offset:4168
	v_cvt_pk_bf16_f32 v0, v19, v59
	ds_write_b32 v140, v0 offset:4172
	v_cvt_pk_bf16_f32 v0, v20, v60
	ds_write_b32 v140, v0 offset:5200
	v_cvt_pk_bf16_f32 v0, v21, v61
	ds_write_b32 v140, v0 offset:5204
	v_cvt_pk_bf16_f32 v0, v22, v62
	ds_write_b32 v140, v0 offset:5208
	v_cvt_pk_bf16_f32 v0, v23, v63
	ds_write_b32 v140, v0 offset:5212
	v_cvt_pk_bf16_f32 v0, v36, v40
	ds_write_b32 v140, v0 offset:6240
	v_cvt_pk_bf16_f32 v0, v37, v41
	ds_write_b32 v140, v0 offset:6244
	v_cvt_pk_bf16_f32 v0, v38, v42
	s_lshr_b32 s2, s21, 6
	ds_write_b32 v140, v0 offset:6248
	v_cvt_f32_u32_e32 v0, s2
	s_sub_i32 s30, 0, s2
	s_abs_i32 s29, s17
	s_ashr_i32 s21, s17, 31
	v_rcp_iflag_f32_e32 v0, v0
	v_cvt_pk_bf16_f32 v1, v39, v43
	ds_write_b32 v140, v1 offset:6252
	v_cvt_pk_bf16_f32 v1, v28, v24
	v_mul_f32_e32 v0, 0x4f7ffffe, v0
	v_cvt_u32_f32_e32 v0, v0
	ds_write_b32 v140, v1 offset:7280
	v_cvt_pk_bf16_f32 v1, v29, v25
	ds_write_b32 v140, v1 offset:7284
	v_readfirstlane_b32 s4, v0
	s_mul_i32 s30, s30, s4
	s_mul_hi_u32 s30, s4, s30
	s_add_i32 s4, s4, s30
	s_mul_hi_u32 s4, s29, s4
	s_mul_i32 s30, s4, s2
	s_sub_i32 s29, s29, s30
	s_add_i32 s30, s4, 1
	s_sub_i32 s31, s29, s2
	s_cmp_ge_u32 s29, s2
	s_cselect_b32 s4, s30, s4
	s_cselect_b32 s29, s31, s29
	s_add_i32 s30, s4, 1
	s_cmp_ge_u32 s29, s2
	s_cselect_b32 s4, s30, s4
	s_xor_b32 s4, s4, s21
	s_sub_i32 s4, s4, s21
	s_mul_i32 s2, s4, s2
	v_cvt_pk_bf16_f32 v1, v30, v26
	s_sub_i32 s2, s17, s2
	ds_write_b32 v140, v1 offset:7288
	v_cvt_pk_bf16_f32 v1, v31, v27
	ds_write_b32 v140, v1 offset:7292
	s_lshl_b32 s17, s2, 6
	s_ashr_i32 s2, s2, 2
	s_waitcnt lgkmcnt(0)
	s_mul_i32 s2, s2, s40
	s_add_i32 s4, s4, s41
	s_add_i32 s30, s4, s2
	ds_read2_b32 v[8:9], v134 offset1:8
	ds_read2_b32 v[0:1], v134 offset0:65 offset1:73
	ds_read2_b32 v[10:11], v134 offset0:130 offset1:138
	ds_read2_b32 v[2:3], v134 offset0:195 offset1:203
	s_ashr_i32 s31, s30, 31
	s_and_b32 s17, s17, 0xc0
	s_lshl_b64 s[30:31], s[30:31], 15
	s_add_u32 s14, s14, s30
	v_add_lshl_u32 v12, s17, v132, 6
	s_addc_u32 s15, s15, s31
	v_ashrrev_i32_e32 v13, 31, v12
	v_lshl_add_u64 v[12:13], v[12:13], 1, s[14:15]
	s_waitcnt lgkmcnt(3)
	v_mov_b32_e32 v4, v8
	s_waitcnt lgkmcnt(2)
	v_mov_b32_e32 v5, v0
	s_waitcnt lgkmcnt(1)
	v_mov_b32_e32 v6, v10
	s_waitcnt lgkmcnt(0)
	v_mov_b32_e32 v7, v2
	v_lshl_add_u64 v[12:13], v[12:13], 0, v[130:131]
	global_store_dwordx4 v[12:13], v[4:7], off nt
	v_mov_b32_e32 v0, v9
	v_mov_b32_e32 v2, v11
	v_add_lshl_u32 v4, s17, v135, 6
	v_ashrrev_i32_e32 v5, 31, v4
	v_lshl_add_u64 v[4:5], v[4:5], 1, s[14:15]
	v_lshl_add_u64 v[8:9], v[4:5], 0, v[130:131]
	ds_read2_b32 v[10:11], v134 offset0:16 offset1:24
	ds_read2_b32 v[4:5], v134 offset0:81 offset1:89
	ds_read2_b32 v[12:13], v134 offset0:146 offset1:154
	ds_read2_b32 v[6:7], v134 offset0:211 offset1:219
	global_store_dwordx4 v[8:9], v[0:3], off nt
	v_add_lshl_u32 v8, s17, v136, 6
	v_ashrrev_i32_e32 v9, 31, v8
	v_lshl_add_u64 v[8:9], v[8:9], 1, s[14:15]
	s_waitcnt lgkmcnt(3)
	v_mov_b32_e32 v0, v10
	s_waitcnt lgkmcnt(2)
	v_mov_b32_e32 v1, v4
	s_waitcnt lgkmcnt(1)
	v_mov_b32_e32 v2, v12
	s_waitcnt lgkmcnt(0)
	v_mov_b32_e32 v3, v6
	v_lshl_add_u64 v[8:9], v[8:9], 0, v[130:131]
	global_store_dwordx4 v[8:9], v[0:3], off nt
	v_mov_b32_e32 v4, v11
	v_mov_b32_e32 v6, v13
	v_add_lshl_u32 v0, s17, v137, 6
	v_ashrrev_i32_e32 v1, 31, v0
	v_lshl_add_u64 v[0:1], v[0:1], 1, s[14:15]
	v_lshl_add_u64 v[8:9], v[0:1], 0, v[130:131]
	ds_read2_b32 v[10:11], v134 offset0:32 offset1:40
	ds_read2_b32 v[0:1], v134 offset0:97 offset1:105
	ds_read2_b32 v[12:13], v134 offset0:162 offset1:170
	ds_read2_b32 v[2:3], v134 offset0:227 offset1:235
	global_store_dwordx4 v[8:9], v[4:7], off nt
	v_add_lshl_u32 v8, s17, v138, 6
	v_ashrrev_i32_e32 v9, 31, v8
	v_lshl_add_u64 v[8:9], v[8:9], 1, s[14:15]
	s_waitcnt lgkmcnt(3)
	v_mov_b32_e32 v4, v10
	s_waitcnt lgkmcnt(2)
	v_mov_b32_e32 v5, v0
	s_waitcnt lgkmcnt(1)
	v_mov_b32_e32 v6, v12
	s_waitcnt lgkmcnt(0)
	v_mov_b32_e32 v7, v2
	v_lshl_add_u64 v[8:9], v[8:9], 0, v[130:131]
	global_store_dwordx4 v[8:9], v[4:7], off nt
	v_mov_b32_e32 v0, v11
	v_mov_b32_e32 v2, v13
	v_add_lshl_u32 v4, s17, v139, 6
	v_ashrrev_i32_e32 v5, 31, v4
	v_lshl_add_u64 v[4:5], v[4:5], 1, s[14:15]
	v_lshl_add_u64 v[8:9], v[4:5], 0, v[130:131]
	ds_read2_b32 v[10:11], v134 offset0:48 offset1:56
	ds_read2_b32 v[4:5], v134 offset0:113 offset1:121
	ds_read2_b32 v[12:13], v134 offset0:178 offset1:186
	ds_read2_b32 v[6:7], v134 offset0:243 offset1:251
	global_store_dwordx4 v[8:9], v[0:3], off nt
	v_add_lshl_u32 v8, s17, v141, 6
	v_ashrrev_i32_e32 v9, 31, v8
	v_lshl_add_u64 v[8:9], v[8:9], 1, s[14:15]
	s_waitcnt lgkmcnt(3)
	v_mov_b32_e32 v0, v10
	s_waitcnt lgkmcnt(2)
	v_mov_b32_e32 v1, v4
	s_waitcnt lgkmcnt(1)
	v_mov_b32_e32 v2, v12
	s_waitcnt lgkmcnt(0)
	v_mov_b32_e32 v3, v6
	v_lshl_add_u64 v[8:9], v[8:9], 0, v[130:131]
	global_store_dwordx4 v[8:9], v[0:3], off nt
	v_mov_b32_e32 v4, v11
	v_mov_b32_e32 v6, v13
	v_add_lshl_u32 v0, s17, v142, 6
	v_ashrrev_i32_e32 v1, 31, v0
	v_lshl_add_u64 v[0:1], v[0:1], 1, s[14:15]
	v_lshl_add_u64 v[0:1], v[0:1], 0, v[130:131]
	global_store_dwordx4 v[0:1], v[4:7], off nt
	s_waitcnt lgkmcnt(0)
	s_add_i32 s22, s22, s25
	s_min_i32 s4, s22, s24
	s_cmpk_gt_i32 s4, 0x1fff
	s_mov_b64 s[34:35], -1
	s_cbranch_scc0 .LBB0_67
	s_cmpk_gt_u32 s4, 0x23ff
	s_cbranch_scc0 .LBB0_64
	s_cmpk_gt_u32 s4, 0x27ff
	s_cbranch_scc0 .LBB0_62
	s_cmpk_gt_u32 s4, 0x2bff
	s_cbranch_scc0 .LBB0_59
	s_cmp_gt_u32 s4, 0x12bff
	s_cbranch_scc0 .LBB0_56
	s_load_dwordx2 s[14:15], s[12:13], 0xa8
	s_add_i32 s2, s4, 0xfffed400
	s_lshr_b32 s2, s2, 10
	s_lshl_b64 s[30:31], s[2:3], 24
	s_mov_b64 s[34:35], 0
	s_waitcnt lgkmcnt(0)
	s_add_u32 s30, s14, s30
	s_addc_u32 s31, s15, s31
	s_lshl_b64 s[14:15], s[2:3], 23
	s_add_u32 s14, s18, s14
	s_addc_u32 s15, s19, s15
	s_and_b32 s17, s4, 0x3ff

; #define GAS __attribute__((address_space(1)))
; #define LAS __attribute__((address_space(3)))
; __device__ __forceinline__ void conv_load(const ConvSrc& c, int lane, f32x4 (&ra)[8], f32x4 (&rb)[8]) {
;     const int nblk = c.N >> 6, kb = c.kfast ? (c.item & 31) : c.item / nblk, nb = c.kfast ? (c.item >> 5) : c.item - kb * nblk, k0 = kb * 64, n0 = nb * 64;
;     const int n4 = (lane & 15) * 4, kq = lane >> 4;
; #pragma unroll
;     for (int i = 0; i < 8; ++i) { const int kp2 = 4 * i + kq; const float* p = c.W + (size_t)(k0 + 2 * kp2) * c.N + n0 + n4; ra[i] = __builtin_nontemporal_load((const GAS f32x4*)p); rb[i] = __builtin_nontemporal_load((const GAS f32x4*)(p + c.N)); }
; }
; __device__ __forceinline__ void conv_run(KP kp, unsigned char* ws, LAS unsigned* P, int lane, int first, int it_hi, int step) {
;     if (first >= it_hi) return;
;     const int lastv = first + ((it_hi - 1 - first) / step) * step;
;     f32x4 a0[8], b0[8], a1[8], b1[8];
;     ConvSrc c0 = conv_decode(kp, ws, first), c1;
;     conv_load(c0, lane, a0, b0);
.LBB0_613:
	s_lshr_b32 s19, s6, 6
	v_cvt_f32_u32_e32 v0, s19
	s_sub_i32 s20, 0, s19
	s_abs_i32 s5, s69
	s_ashr_i32 s4, s69, 31
	v_rcp_iflag_f32_e32 v0, v0
	v_ashrrev_i32_e32 v131, 3, v66
	v_and_b32_e32 v133, -2, v131
	v_lshlrev_b32_e32 v2, 2, v66
	v_mul_f32_e32 v0, 0x4f7ffffe, v0
	v_cvt_u32_f32_e32 v0, v0
	v_and_b32_e32 v130, 60, v2
	v_ashrrev_i32_e32 v67, 4, v66
	v_and_b32_e32 v66, 7, v66
	v_readfirstlane_b32 s21, v0
	s_mul_i32 s20, s20, s21
	s_mul_hi_u32 s20, s21, s20
	s_add_i32 s21, s21, s20
	s_mul_hi_u32 s20, s5, s21
	s_mul_i32 s21, s20, s19
	s_sub_i32 s5, s5, s21
	s_add_i32 s23, s20, 1
	s_sub_i32 s21, s5, s19
	s_cmp_ge_u32 s5, s19
	s_cselect_b32 s20, s23, s20
	s_cselect_b32 s5, s21, s5
	s_add_i32 s21, s20, 1
	s_cmp_ge_u32 s5, s19
	s_cselect_b32 s5, s21, s20
	s_xor_b32 s5, s5, s4
	s_sub_i32 s20, s5, s4
	v_lshl_add_u32 v42, s20, 6, v133
	v_add_u32_e32 v0, 56, v42
	v_mad_u64_u32 v[2:3], s[4:5], v0, s6, 0
	v_ashrrev_i32_e32 v4, 31, v0
	v_mov_b32_e32 v0, v3
	v_mad_u64_u32 v[4:5], s[4:5], v4, s6, v[0:1]
	s_mul_i32 s20, s20, s19
	s_sub_i32 s4, s69, s20
	s_lshl_b32 s4, s4, 6
	v_mov_b32_e32 v3, v4
	s_ashr_i32 s5, s4, 31
	s_waitcnt lgkmcnt(0)
	v_lshl_add_u64 v[2:3], v[2:3], 2, s[56:57]
	s_lshl_b64 s[60:61], s[4:5], 2
	v_lshl_add_u64 v[2:3], v[2:3], 0, s[60:61]
	v_lshlrev_b32_e32 v0, 2, v130
	v_add_u32_e32 v10, 16, v42
	v_add_u32_e32 v18, 32, v42
	v_lshl_add_u64 v[26:27], v[2:3], 0, v[0:1]
	v_mad_u64_u32 v[2:3], s[4:5], v42, s6, 0
	v_ashrrev_i32_e32 v13, 31, v10
	v_mad_u64_u32 v[10:11], s[4:5], v10, s6, 0
	v_ashrrev_i32_e32 v21, 31, v18
	v_mad_u64_u32 v[18:19], s[4:5], v18, s6, 0
	v_ashrrev_i32_e32 v5, 31, v42
	v_mov_b32_e32 v4, v3
	v_mov_b32_e32 v12, v11
	v_mov_b32_e32 v20, v19
	v_mad_u64_u32 v[4:5], s[4:5], v5, s6, v[4:5]
	v_mad_u64_u32 v[12:13], s[4:5], v13, s6, v[12:13]
	v_mad_u64_u32 v[20:21], s[4:5], v21, s6, v[20:21]
	v_mov_b32_e32 v3, v4
	v_mov_b32_e32 v11, v12
	v_mov_b32_e32 v19, v20
	v_lshl_add_u64 v[2:3], v[2:3], 2, s[56:57]
	v_lshl_add_u64 v[10:11], v[10:11], 2, s[56:57]
	v_lshl_add_u64 v[18:19], v[18:19], 2, s[56:57]
	v_lshl_add_u64 v[2:3], v[2:3], 0, s[60:61]
	v_lshl_add_u64 v[10:11], v[10:11], 0, s[60:61]
	v_lshl_add_u64 v[18:19], v[18:19], 0, s[60:61]
	v_lshl_add_u64 v[34:35], v[2:3], 0, v[0:1]
	v_add_u32_e32 v2, 8, v42
	v_lshl_add_u64 v[30:31], v[10:11], 0, v[0:1]
	v_add_u32_e32 v10, 24, v42
	v_lshl_add_u64 v[38:39], v[18:19], 0, v[0:1]
	v_add_u32_e32 v18, 40, v42
	v_add_u32_e32 v42, 48, v42
	v_ashrrev_i32_e32 v45, 31, v42
	v_mad_u64_u32 v[42:43], s[4:5], v42, s6, 0
	v_ashrrev_i32_e32 v5, 31, v2
	v_mad_u64_u32 v[2:3], s[4:5], v2, s6, 0
	v_ashrrev_i32_e32 v13, 31, v10
	v_mad_u64_u32 v[10:11], s[4:5], v10, s6, 0
	v_ashrrev_i32_e32 v21, 31, v18
	v_mad_u64_u32 v[18:19], s[4:5], v18, s6, 0
	v_mov_b32_e32 v44, v43
	v_mov_b32_e32 v4, v3
	v_mov_b32_e32 v12, v11
	v_mov_b32_e32 v20, v19
	v_mad_u64_u32 v[44:45], s[4:5], v45, s6, v[44:45]
	v_mad_u64_u32 v[4:5], s[4:5], v5, s6, v[4:5]
	v_mad_u64_u32 v[12:13], s[4:5], v13, s6, v[12:13]
	v_mad_u64_u32 v[20:21], s[4:5], v21, s6, v[20:21]
	v_mov_b32_e32 v43, v44
	v_mov_b32_e32 v3, v4
	v_mov_b32_e32 v11, v12
	v_mov_b32_e32 v19, v20
	v_lshl_add_u64 v[42:43], v[42:43], 2, s[56:57]
	s_lshl_b64 s[58:59], s[6:7], 2
	v_lshl_add_u64 v[2:3], v[2:3], 2, s[56:57]
	v_lshl_add_u64 v[10:11], v[10:11], 2, s[56:57]
	v_lshl_add_u64 v[18:19], v[18:19], 2, s[56:57]
	v_lshl_add_u64 v[42:43], v[42:43], 0, s[60:61]
	v_lshl_add_u64 v[28:29], v[26:27], 0, s[58:59]
	v_lshl_add_u64 v[2:3], v[2:3], 0, s[60:61]
	v_lshl_add_u64 v[10:11], v[10:11], 0, s[60:61]
	v_lshl_add_u64 v[18:19], v[18:19], 0, s[60:61]
	v_lshl_add_u64 v[42:43], v[42:43], 0, v[0:1]
	v_lshl_add_u64 v[36:37], v[2:3], 0, v[0:1]
	global_load_dwordx4 v[2:5], v[34:35], off nt
	global_load_dwordx4 v[6:9], v[36:37], off nt
	v_lshl_add_u64 v[32:33], v[10:11], 0, v[0:1]
	global_load_dwordx4 v[10:13], v[30:31], off nt
	global_load_dwordx4 v[14:17], v[32:33], off nt
	v_lshl_add_u64 v[40:41], v[18:19], 0, v[0:1]
	global_load_dwordx4 v[18:21], v[38:39], off nt
	global_load_dwordx4 v[22:25], v[40:41], off nt
	global_load_dwordx4 v[50:53], v[28:29], off nt
	global_load_dwordx4 v[54:57], v[26:27], off nt
	v_lshl_add_u64 v[26:27], v[42:43], 0, s[58:59]
	global_load_dwordx4 v[46:49], v[42:43], off nt
	global_load_dwordx4 v[58:61], v[26:27], off nt
	v_lshl_add_u64 v[26:27], v[40:41], 0, s[58:59]
	v_lshl_add_u64 v[28:29], v[38:39], 0, s[58:59]
	global_load_dwordx4 v[62:65], v[26:27], off nt
	global_load_dwordx4 v[38:41], v[28:29], off nt
	v_lshl_add_u64 v[26:27], v[32:33], 0, s[58:59]
	v_lshl_add_u64 v[28:29], v[30:31], 0, s[58:59]
	global_load_dwordx4 v[42:45], v[26:27], off nt
	global_load_dwordx4 v[30:33], v[28:29], off nt
	v_lshl_add_u64 v[26:27], v[36:37], 0, s[58:59]
	v_lshl_add_u64 v[28:29], v[34:35], 0, s[58:59]
	global_load_dwordx4 v[34:37], v[26:27], off nt
	s_nop 0
	global_load_dwordx4 v[26:29], v[28:29], off nt
	s_movk_i32 s4, 0x104
	v_add_u32_e32 v0, s68, v0
	v_mul_lo_u32 v67, v67, s4
	v_mul_u32_u24_e32 v68, 0x410, v66
	v_lshlrev_b32_e32 v132, 3, v66
	v_lshlrev_b32_e32 v66, 2, v131
	v_add3_u32 v136, s68, v68, v66
	v_add_u32_e32 v137, 8, v131
	v_add_u32_e32 v138, 16, v131
	v_add_u32_e32 v139, 24, v131
	v_add_u32_e32 v140, 32, v131
	v_add_u32_e32 v141, 40, v131
	v_add_u32_e32 v142, 48, v131
	v_add_u32_e32 v143, 56, v131
	v_add_u32_e32 v144, v0, v67
	s_mov_b32 s23, s18
	s_mov_b32 s4, s6
	s_mov_b32 s98, 0
	s_branch .LBB0_615

; #define GAS __attribute__((address_space(1)))
; __device__ __forceinline__ void conv_load(const ConvSrc& c, int lane, f32x4 (&ra)[8], f32x4 (&rb)[8]) {
;     const int nblk = c.N >> 6, kb = c.kfast ? (c.item & 31) : c.item / nblk, nb = c.kfast ? (c.item >> 5) : c.item - kb * nblk, k0 = kb * 64, n0 = nb * 64;
;     const int n4 = (lane & 15) * 4, kq = lane >> 4;
; #pragma unroll
;     for (int i = 0; i < 8; ++i) { const int kp2 = 4 * i + kq; const float* p = c.W + (size_t)(k0 + 2 * kp2) * c.N + n0 + n4; ra[i] = __builtin_nontemporal_load((const GAS f32x4*)p); rb[i] = __builtin_nontemporal_load((const GAS f32x4*)(p + c.N)); }
; }
; __device__ __forceinline__ void conv_run(KP kp, unsigned char* ws, LAS unsigned* P, int lane, int first, int it_hi, int step) {
;     ...
;         c1 = conv_decode(kp, ws, min(it + step, lastv)); conv_load(c1, lane, a1, b1);
.LBB0_634:
	s_lshr_b32 s58, s6, 6
	v_cvt_f32_u32_e32 v0, s58
	s_sub_i32 s62, 0, s58
	s_abs_i32 s59, s21
	s_ashr_i32 s20, s21, 31
	v_rcp_iflag_f32_e32 v0, v0
	v_mov_b32_e32 v135, v1
	v_mul_f32_e32 v0, 0x4f7ffffe, v0
	v_cvt_u32_f32_e32 v0, v0
	s_nop 0
	v_readfirstlane_b32 s63, v0
	s_mul_i32 s62, s62, s63
	s_mul_hi_u32 s62, s63, s62
	s_add_i32 s63, s63, s62
	s_mul_hi_u32 s62, s59, s63
	s_mul_i32 s63, s62, s58
	s_sub_i32 s59, s59, s63
	s_add_i32 s63, s62, 1
	s_sub_i32 s64, s59, s58
	s_cmp_ge_u32 s59, s58
	s_cselect_b32 s62, s63, s62
	s_cselect_b32 s59, s64, s59
	s_add_i32 s63, s62, 1
	s_cmp_ge_u32 s59, s58
	s_cselect_b32 s59, s63, s62
	s_xor_b32 s59, s59, s20
	s_sub_i32 s20, s59, s20
	v_lshl_add_u32 v120, s20, 6, v133
	s_mul_i32 s58, s20, s58
	v_mad_u64_u32 v[66:67], s[62:63], v120, s6, 0
	s_sub_i32 s21, s21, s58
	v_ashrrev_i32_e32 v68, 31, v120
	v_mov_b32_e32 v0, v67
	s_lshl_b32 s58, s21, 6
	v_mad_u64_u32 v[68:69], s[62:63], v68, s6, v[0:1]
	s_ashr_i32 s59, s58, 31
	v_mov_b32_e32 v67, v68
	s_waitcnt lgkmcnt(0)
	v_lshl_add_u64 v[66:67], v[66:67], 2, s[60:61]
	s_lshl_b64 s[62:63], s[58:59], 2
	v_lshl_add_u64 v[66:67], v[66:67], 0, s[62:63]
	v_lshlrev_b32_e32 v0, 2, v130
	v_lshl_add_u64 v[70:71], v[66:67], 0, v[0:1]
	s_lshl_b64 s[64:65], s[6:7], 2
	global_load_dwordx4 v[66:69], v[70:71], off nt
	v_lshl_add_u64 v[70:71], v[70:71], 0, s[64:65]
	global_load_dwordx4 v[74:77], v[70:71], off nt
	v_add_u32_e32 v70, 8, v120
	v_ashrrev_i32_e32 v73, 31, v70
	v_mad_u64_u32 v[70:71], vcc, v70, s6, 0
	v_mov_b32_e32 v72, v71
	v_mad_u64_u32 v[72:73], vcc, v73, s6, v[72:73]
	v_mov_b32_e32 v71, v72
	v_lshl_add_u64 v[70:71], v[70:71], 2, s[60:61]
	v_lshl_add_u64 v[70:71], v[70:71], 0, s[62:63]
	v_lshl_add_u64 v[78:79], v[70:71], 0, v[0:1]
	global_load_dwordx4 v[70:73], v[78:79], off nt
	v_lshl_add_u64 v[78:79], v[78:79], 0, s[64:65]
	global_load_dwordx4 v[82:85], v[78:79], off nt
	v_add_u32_e32 v78, 16, v120
	v_ashrrev_i32_e32 v81, 31, v78
	v_mad_u64_u32 v[78:79], vcc, v78, s6, 0
	v_mov_b32_e32 v80, v79
	v_mad_u64_u32 v[80:81], vcc, v81, s6, v[80:81]
	v_mov_b32_e32 v79, v80
	v_lshl_add_u64 v[78:79], v[78:79], 2, s[60:61]
	v_lshl_add_u64 v[78:79], v[78:79], 0, s[62:63]
	v_lshl_add_u64 v[86:87], v[78:79], 0, v[0:1]
	global_load_dwordx4 v[78:81], v[86:87], off nt
	v_lshl_add_u64 v[86:87], v[86:87], 0, s[64:65]
	global_load_dwordx4 v[90:93], v[86:87], off nt
	v_add_u32_e32 v86, 24, v120
	v_ashrrev_i32_e32 v89, 31, v86
	v_mad_u64_u32 v[86:87], vcc, v86, s6, 0
	v_mov_b32_e32 v88, v87
	v_mad_u64_u32 v[88:89], vcc, v89, s6, v[88:89]
	v_mov_b32_e32 v87, v88
	v_lshl_add_u64 v[86:87], v[86:87], 2, s[60:61]
	v_lshl_add_u64 v[86:87], v[86:87], 0, s[62:63]
	v_lshl_add_u64 v[94:95], v[86:87], 0, v[0:1]
	global_load_dwordx4 v[86:89], v[94:95], off nt
	v_lshl_add_u64 v[94:95], v[94:95], 0, s[64:65]
	global_load_dwordx4 v[98:101], v[94:95], off nt
	v_add_u32_e32 v94, 32, v120
	v_ashrrev_i32_e32 v97, 31, v94
	v_mad_u64_u32 v[94:95], vcc, v94, s6, 0
	v_mov_b32_e32 v96, v95
	v_mad_u64_u32 v[96:97], vcc, v97, s6, v[96:97]
	v_mov_b32_e32 v95, v96
	v_lshl_add_u64 v[94:95], v[94:95], 2, s[60:61]
	v_lshl_add_u64 v[94:95], v[94:95], 0, s[62:63]
	v_lshl_add_u64 v[102:103], v[94:95], 0, v[0:1]
	global_load_dwordx4 v[94:97], v[102:103], off nt
	v_lshl_add_u64 v[102:103], v[102:103], 0, s[64:65]
	global_load_dwordx4 v[106:109], v[102:103], off nt
	v_add_u32_e32 v102, 40, v120
	v_ashrrev_i32_e32 v105, 31, v102
	v_mad_u64_u32 v[102:103], vcc, v102, s6, 0
	v_mov_b32_e32 v104, v103
	v_mad_u64_u32 v[104:105], vcc, v105, s6, v[104:105]
	v_mov_b32_e32 v103, v104
	v_lshl_add_u64 v[102:103], v[102:103], 2, s[60:61]
	v_lshl_add_u64 v[102:103], v[102:103], 0, s[62:63]
	v_lshl_add_u64 v[110:111], v[102:103], 0, v[0:1]
	global_load_dwordx4 v[102:105], v[110:111], off nt
	v_lshl_add_u64 v[110:111], v[110:111], 0, s[64:65]
	global_load_dwordx4 v[114:117], v[110:111], off nt
	v_add_u32_e32 v110, 48, v120
	v_ashrrev_i32_e32 v113, 31, v110
	v_mad_u64_u32 v[110:111], vcc, v110, s6, 0
	v_mov_b32_e32 v112, v111
	v_mad_u64_u32 v[112:113], vcc, v113, s6, v[112:113]
	v_mov_b32_e32 v111, v112
	v_lshl_add_u64 v[110:111], v[110:111], 2, s[60:61]
	v_lshl_add_u64 v[110:111], v[110:111], 0, s[62:63]
	v_lshl_add_u64 v[118:119], v[110:111], 0, v[0:1]
	global_load_dwordx4 v[110:113], v[118:119], off nt
	v_lshl_add_u64 v[118:119], v[118:119], 0, s[64:65]
	global_load_dwordx4 v[126:129], v[118:119], off nt
	v_add_u32_e32 v118, 56, v120
	v_ashrrev_i32_e32 v121, 31, v118
	v_mad_u64_u32 v[118:119], vcc, v118, s6, 0
	v_mov_b32_e32 v120, v119
	v_mad_u64_u32 v[120:121], vcc, v121, s6, v[120:121]
	v_mov_b32_e32 v119, v120
	v_lshl_add_u64 v[118:119], v[118:119], 2, s[60:61]
	v_lshl_add_u64 v[118:119], v[118:119], 0, s[62:63]
	v_lshl_add_u64 v[122:123], v[118:119], 0, v[0:1]
	global_load_dwordx4 v[118:121], v[122:123], off nt
	v_lshl_add_u64 v[122:123], v[122:123], 0, s[64:65]
	global_load_dwordx4 v[122:125], v[122:123], off nt
	s_lshr_b32 s4, s4, 6
	s_cmp_eq_u32 s98, 0
	s_cbranch_scc1 .Lcw_first_2
	s_waitcnt vmcnt(24)
	s_branch .Lcw_done_2

; #define GAS __attribute__((address_space(1)))
; #define LAS __attribute__((address_space(3)))
; __device__ __forceinline__ ConvSrc conv_decode(KP kp, unsigned char* ws, int it) {
;     constexpr int I_IN = 32 * 256, I_SQ = 32 * 32, I_UP = 32 * 64, I_DN = 32 * 32;
;     ConvSrc c; int r = it; c.ldk = 2048; c.kfast = 0; c.tiled = 32; c.ktoff = 0;
;     if (r < I_IN) { c.W = (const float*)KIN(6); c.WT = (bf16*)(ws + WS_WIN); c.N = 16384; c.item = r; return c; } r -= I_IN;
;     if (r < I_SQ) { c.W = (const float*)KIN(13); c.WT = (bf16*)(ws + WS_WAO); c.N = 2048; c.item = r; c.ldk = 4096; c.tiled = 64; return c; } r -= I_SQ;
;     if (r < I_SQ) { c.W = (const float*)KIN(14); c.WT = (bf16*)(ws + WS_WAO); c.N = 2048; c.item = r; c.ldk = 4096; c.tiled = 64; c.ktoff = 32; return c; } r -= I_SQ;
;     if (r < I_SQ) { c.W = (const float*)KIN(15); c.WT = (bf16*)(ws + WS_WO); c.N = 2048; c.item = r; return c; } r -= I_SQ;
;     if (r < NE * I_UP) { const int e = r / I_UP; c.W = (const float*)KIN(19) + (size_t)e * 2048 * 4096; c.WT = (bf16*)(ws + WS_WUP) + (size_t)e * 4096 * 2048; c.N = 4096; c.item = r - e * I_UP; return c; } r -= NE * I_UP;
; __device__ __forceinline__ void conv_emit(const ConvSrc& c, int lane, LAS unsigned* P, const f32x4 (&ra)[8], const f32x4 (&rb)[8]) {
;     const int nblk = c.N >> 6, kb = c.kfast ? (c.item & 31) : c.item / nblk, nb = c.kfast ? (c.item >> 5) : c.item - kb * nblk, k0 = kb * 64, n0 = nb * 64;
;     const int n4 = (lane & 15) * 4, kq = lane >> 4;
; #pragma unroll
;     for (int i = 0; i < 8; ++i) { const int kp2 = 4 * i + kq; LAS unsigned* d = P + kp2 * 65 + n4;
;         d[0] = pg8::cvt_pk_bf16(ra[i].x, rb[i].x); d[1] = pg8::cvt_pk_bf16(ra[i].y, rb[i].y); d[2] = pg8::cvt_pk_bf16(ra[i].z, rb[i].z); d[3] = pg8::cvt_pk_bf16(ra[i].w, rb[i].w); }
;     LDS_WAIT(); asm volatile("" ::: "memory");
;     const int cc = lane & 7;
; #pragma unroll
;     for (int jj = 0; jj < 8; ++jj) { const int n = (lane >> 3) + 8 * jj; const LAS unsigned* sp = P + (4 * cc) * 65 + n;
;         v4u o; o.x = sp[0]; o.y = sp[65]; o.z = sp[130]; o.w = sp[195];
;         bf16* dst = c.tiled ? c.WT + (size_t)((nb >> 2) * c.tiled + c.ktoff + kb) * 16384 + ((nb & 3) * 64 + n) * 64 + 8 * cc : c.WT + (size_t)(n0 + n) * c.ldk + k0 + 8 * cc;
;         __builtin_nontemporal_store(o, (GAS v4u*)dst); }
;     LDS_WAIT(); asm volatile("" ::: "memory");
.Lcw_done_2:
	v_cvt_pk_bf16_f32 v2, v2, v26
	v_cvt_f32_u32_e32 v134, s4
	ds_write_b32 v144, v2
	v_cvt_pk_bf16_f32 v2, v3, v27
	ds_write_b32 v144, v2 offset:4
	v_cvt_pk_bf16_f32 v2, v4, v28
	ds_write_b32 v144, v2 offset:8
	v_cvt_pk_bf16_f32 v2, v5, v29
	ds_write_b32 v144, v2 offset:12
	v_cvt_pk_bf16_f32 v2, v6, v34
	v_rcp_iflag_f32_e32 v134, v134
	ds_write_b32 v144, v2 offset:1040
	v_cvt_pk_bf16_f32 v2, v7, v35
	ds_write_b32 v144, v2 offset:1044
	v_cvt_pk_bf16_f32 v2, v8, v36
	ds_write_b32 v144, v2 offset:1048
	v_cvt_pk_bf16_f32 v2, v9, v37
	ds_write_b32 v144, v2 offset:1052
	v_cvt_pk_bf16_f32 v2, v10, v30
	v_mul_f32_e32 v134, 0x4f7ffffe, v134
	ds_write_b32 v144, v2 offset:2080
	v_cvt_pk_bf16_f32 v2, v11, v31
	v_cvt_u32_f32_e32 v134, v134
	ds_write_b32 v144, v2 offset:2084
	v_cvt_pk_bf16_f32 v2, v12, v32
	ds_write_b32 v144, v2 offset:2088
	v_cvt_pk_bf16_f32 v2, v13, v33
	ds_write_b32 v144, v2 offset:2092
	v_cvt_pk_bf16_f32 v2, v14, v42
	ds_write_b32 v144, v2 offset:3120
	v_cvt_pk_bf16_f32 v2, v15, v43
	s_sub_i32 s60, 0, s4
	v_readfirstlane_b32 s61, v134
	ds_write_b32 v144, v2 offset:3124
	v_cvt_pk_bf16_f32 v2, v16, v44
	s_mul_i32 s60, s60, s61
	ds_write_b32 v144, v2 offset:3128
	v_cvt_pk_bf16_f32 v2, v17, v45
	s_mul_hi_u32 s60, s61, s60
	ds_write_b32 v144, v2 offset:3132
	v_cvt_pk_bf16_f32 v2, v18, v38
	s_abs_i32 s59, s69
	s_add_i32 s61, s61, s60
	ds_write_b32 v144, v2 offset:4160
	v_cvt_pk_bf16_f32 v2, v19, v39
	s_mul_hi_u32 s60, s59, s61
	ds_write_b32 v144, v2 offset:4164
	v_cvt_pk_bf16_f32 v2, v20, v40
	s_mul_i32 s61, s60, s4
	ds_write_b32 v144, v2 offset:4168
	v_cvt_pk_bf16_f32 v2, v21, v41
	s_sub_i32 s59, s59, s61
	ds_write_b32 v144, v2 offset:4172
	v_cvt_pk_bf16_f32 v2, v22, v62
	s_ashr_i32 s6, s69, 31
	s_add_i32 s61, s60, 1
	s_sub_i32 s62, s59, s4
	ds_write_b32 v144, v2 offset:5200
	v_cvt_pk_bf16_f32 v2, v23, v63
	s_cmp_ge_u32 s59, s4
	ds_write_b32 v144, v2 offset:5204
	v_cvt_pk_bf16_f32 v2, v24, v64
	s_cselect_b32 s60, s61, s60
	ds_write_b32 v144, v2 offset:5208
	v_cvt_pk_bf16_f32 v2, v25, v65
	s_cselect_b32 s59, s62, s59
	s_add_i32 s61, s60, 1
	ds_write_b32 v144, v2 offset:5212
	v_cvt_pk_bf16_f32 v2, v46, v58
	s_cmp_ge_u32 s59, s4
	ds_write_b32 v144, v2 offset:6240
	v_cvt_pk_bf16_f32 v2, v47, v59
	s_cselect_b32 s59, s61, s60
	ds_write_b32 v144, v2 offset:6244
	v_cvt_pk_bf16_f32 v2, v48, v60
	s_xor_b32 s59, s59, s6
	ds_write_b32 v144, v2 offset:6248
	v_cvt_pk_bf16_f32 v2, v49, v61
	s_sub_i32 s6, s59, s6
	ds_write_b32 v144, v2 offset:6252
	v_cvt_pk_bf16_f32 v2, v54, v50
	s_mul_i32 s4, s6, s4
	ds_write_b32 v144, v2 offset:7280
	v_cvt_pk_bf16_f32 v2, v55, v51
	s_sub_i32 s4, s69, s4
	ds_write_b32 v144, v2 offset:7284
	v_cvt_pk_bf16_f32 v2, v56, v52
	ds_write_b32 v144, v2 offset:7288
	v_cvt_pk_bf16_f32 v2, v57, v53
	ds_write_b32 v144, v2 offset:7292
	s_ashr_i32 s60, s4, 2
	s_waitcnt lgkmcnt(0)
	s_mul_i32 s60, s60, s17
	s_add_i32 s6, s6, s66
	s_add_i32 s60, s6, s60
	s_lshl_b32 s59, s4, 6
	ds_read2_b32 v[2:3], v136 offset0:65 offset1:73
	ds_read2_b32 v[10:11], v136 offset0:130 offset1:138
	ds_read2_b32 v[4:5], v136 offset0:195 offset1:203
	ds_read2_b32 v[12:13], v136 offset1:8
	s_ashr_i32 s61, s60, 31
	s_and_b32 s4, s59, 0xc0
	s_lshl_b64 s[60:61], s[60:61], 15
	s_add_u32 s54, s54, s60
	v_add_lshl_u32 v14, s4, v131, 6
	s_addc_u32 s55, s55, s61
	v_ashrrev_i32_e32 v15, 31, v14
	v_lshl_add_u64 v[14:15], v[14:15], 1, s[54:55]
	v_lshlrev_b32_e32 v134, 1, v132
	s_waitcnt lgkmcnt(0)
	v_mov_b32_e32 v6, v12
	v_mov_b32_e32 v7, v2
	v_mov_b32_e32 v8, v10
	v_mov_b32_e32 v9, v4
	v_lshl_add_u64 v[14:15], v[14:15], 0, v[134:135]
	global_store_dwordx4 v[14:15], v[6:9], off nt
	v_mov_b32_e32 v2, v13
	v_mov_b32_e32 v4, v11
	v_add_lshl_u32 v6, s4, v137, 6
	v_ashrrev_i32_e32 v7, 31, v6
	v_lshl_add_u64 v[6:7], v[6:7], 1, s[54:55]
	v_lshl_add_u64 v[6:7], v[6:7], 0, v[134:135]
	global_store_dwordx4 v[6:7], v[2:5], off nt
	ds_read2_b32 v[10:11], v136 offset0:16 offset1:24
	ds_read2_b32 v[2:3], v136 offset0:81 offset1:89
	ds_read2_b32 v[12:13], v136 offset0:146 offset1:154
	ds_read2_b32 v[4:5], v136 offset0:211 offset1:219
	v_add_lshl_u32 v14, s4, v138, 6
	v_ashrrev_i32_e32 v15, 31, v14
	v_lshl_add_u64 v[14:15], v[14:15], 1, s[54:55]
	s_waitcnt lgkmcnt(3)
	v_mov_b32_e32 v6, v10
	s_waitcnt lgkmcnt(2)
	v_mov_b32_e32 v7, v2
	s_waitcnt lgkmcnt(1)
	v_mov_b32_e32 v8, v12
	s_waitcnt lgkmcnt(0)
	v_mov_b32_e32 v9, v4
	v_lshl_add_u64 v[14:15], v[14:15], 0, v[134:135]
	global_store_dwordx4 v[14:15], v[6:9], off nt
	v_mov_b32_e32 v2, v11
	v_mov_b32_e32 v4, v13
	v_add_lshl_u32 v6, s4, v139, 6
	v_ashrrev_i32_e32 v7, 31, v6
	v_lshl_add_u64 v[6:7], v[6:7], 1, s[54:55]
	v_lshl_add_u64 v[6:7], v[6:7], 0, v[134:135]
	global_store_dwordx4 v[6:7], v[2:5], off nt
	ds_read2_b32 v[2:3], v136 offset0:97 offset1:105
	ds_read2_b32 v[10:11], v136 offset0:162 offset1:170
	ds_read2_b32 v[4:5], v136 offset0:227 offset1:235
	ds_read2_b32 v[12:13], v136 offset0:32 offset1:40
	v_add_lshl_u32 v14, s4, v140, 6
	v_ashrrev_i32_e32 v15, 31, v14
	v_lshl_add_u64 v[14:15], v[14:15], 1, s[54:55]
	s_waitcnt lgkmcnt(3)
	v_mov_b32_e32 v7, v2
	s_waitcnt lgkmcnt(0)
	v_mov_b32_e32 v6, v12
	v_mov_b32_e32 v8, v10
	v_mov_b32_e32 v9, v4
	v_lshl_add_u64 v[14:15], v[14:15], 0, v[134:135]
	global_store_dwordx4 v[14:15], v[6:9], off nt
	v_mov_b32_e32 v2, v13
	v_mov_b32_e32 v4, v11
	v_add_lshl_u32 v6, s4, v141, 6
	v_ashrrev_i32_e32 v7, 31, v6
	v_lshl_add_u64 v[6:7], v[6:7], 1, s[54:55]
	v_lshl_add_u64 v[6:7], v[6:7], 0, v[134:135]
	global_store_dwordx4 v[6:7], v[2:5], off nt
	ds_read2_b32 v[10:11], v136 offset0:48 offset1:56
	ds_read2_b32 v[2:3], v136 offset0:113 offset1:121
	ds_read2_b32 v[12:13], v136 offset0:178 offset1:186
	ds_read2_b32 v[4:5], v136 offset0:243 offset1:251
	v_add_lshl_u32 v14, s4, v142, 6
	v_ashrrev_i32_e32 v15, 31, v14
	v_lshl_add_u64 v[14:15], v[14:15], 1, s[54:55]
	s_waitcnt lgkmcnt(3)
	v_mov_b32_e32 v6, v10
	s_waitcnt lgkmcnt(2)
	v_mov_b32_e32 v7, v2
	s_waitcnt lgkmcnt(1)
	v_mov_b32_e32 v8, v12
	s_waitcnt lgkmcnt(0)
	v_mov_b32_e32 v9, v4
	v_lshl_add_u64 v[14:15], v[14:15], 0, v[134:135]
	global_store_dwordx4 v[14:15], v[6:9], off nt
	v_mov_b32_e32 v2, v11
	v_mov_b32_e32 v4, v13
	v_add_lshl_u32 v6, s4, v143, 6
	v_ashrrev_i32_e32 v7, 31, v6
	v_lshl_add_u64 v[6:7], v[6:7], 1, s[54:55]
	v_lshl_add_u64 v[6:7], v[6:7], 0, v[134:135]
	global_store_dwordx4 v[6:7], v[2:5], off nt
	s_waitcnt lgkmcnt(0)
	s_add_i32 s23, s23, s73
	s_min_i32 s4, s23, s88
	s_mov_b64 s[62:63], -1
	s_cmpk_gt_i32 s4, 0x1fff
	s_cbranch_scc0 .LBB0_651
	s_cmpk_gt_u32 s4, 0x23ff
	s_cbranch_scc0 .LBB0_648
	s_cmpk_gt_u32 s4, 0x27ff
	s_cbranch_scc0 .LBB0_646
	s_cmpk_gt_u32 s4, 0x2bff
	s_cbranch_scc0 .LBB0_643
	s_cmp_gt_u32 s4, 0x12bff
	s_cbranch_scc0 .LBB0_640
	s_load_dwordx2 s[54:55], s[2:3], 0xa8
	s_add_i32 s6, s4, 0xfffed400
	s_lshr_b32 s6, s6, 10
	s_lshl_b64 s[60:61], s[6:7], 24
	s_mov_b64 s[62:63], 0
	s_waitcnt lgkmcnt(0)
	s_add_u32 s60, s54, s60
	s_addc_u32 s61, s55, s61
	s_lshl_b64 s[54:55], s[6:7], 23
	s_add_u32 s54, s84, s54
	s_addc_u32 s55, s85, s55
	s_and_b32 s69, s4, 0x3ff

; #define LAS __attribute__((address_space(3)))
; __device__ __forceinline__ int fresh_lane() { int l; asm volatile("v_mbcnt_lo_u32_b32 %0, -1, 0\n\tv_mbcnt_hi_u32_b32 %0, -1, %0" : "=v"(l)); return l; }
; __device__ __forceinline__ void conv_run(KP kp, unsigned char* ws, LAS unsigned* P, int lane, int first, int it_hi, int step) {
;     if (first >= it_hi) return;
;     const int lastv = first + ((it_hi - 1 - first) / step) * step;
;     f32x4 a0[8], b0[8], a1[8], b1[8];
;     ConvSrc c0 = conv_decode(kp, ws, first), c1;
;     conv_load(c0, lane, a0, b0);
; __device__ __forceinline__ void conv_moe_range(KP kp, LAS unsigned char* lds, int wave, int lo, int hi) {
;     const int lane = fresh_lane();
;     conv_run(kp, KWS(), (LAS unsigned*)(lds + wave * 8320), lane, lo + wave, hi, NWAVES);
;     __syncthreads();
.LBB0_2246:
	s_lshr_b32 s19, s28, 6
	v_cvt_f32_u32_e32 v0, s19
	s_not_b32 s4, s22
	s_add_i32 s4, s17, s4
	s_sub_i32 s21, 0, s19
	v_rcp_iflag_f32_e32 v0, v0
	s_ashr_i32 s5, s4, 31
	s_lshr_b32 s5, s5, 29
	s_add_i32 s4, s4, s5
	v_mul_f32_e32 v0, 0x4f7ffffe, v0
	v_cvt_u32_f32_e32 v0, v0
	s_abs_i32 s5, s18
	s_and_b32 s23, s4, -8
	s_mul_i32 s4, s82, 0x2080
	v_readfirstlane_b32 s24, v0
	s_mul_i32 s21, s21, s24
	s_mul_hi_u32 s21, s24, s21
	s_add_i32 s24, s24, s21
	s_mul_hi_u32 s21, s5, s24
	s_mul_i32 s24, s21, s19
	s_sub_i32 s5, s5, s24
	s_add_i32 s23, s23, s22
	s_add_i32 s20, s4, 0
	s_ashr_i32 s4, s18, 31
	s_add_i32 s24, s21, 1
	s_sub_i32 s25, s5, s19
	s_cmp_ge_u32 s5, s19
	s_cselect_b32 s21, s24, s21
	s_cselect_b32 s5, s25, s5
	s_add_i32 s24, s21, 1
	s_cmp_ge_u32 s5, s19
	s_cselect_b32 s5, s24, s21
	v_ashrrev_i32_e32 v132, 3, v64
	s_xor_b32 s5, s5, s4
	v_and_b32_e32 v133, -2, v132
	s_sub_i32 s21, s5, s4
	v_lshl_add_u32 v40, s21, 6, v133
	v_lshlrev_b32_e32 v1, 2, v64
	v_add_u32_e32 v0, 56, v40
	v_and_b32_e32 v66, 60, v1
	v_ashrrev_i32_e32 v3, 31, v0
	v_mad_u64_u32 v[0:1], s[4:5], v0, s28, 0
	v_mov_b32_e32 v2, v1
	v_mad_u64_u32 v[2:3], s[4:5], v3, s28, v[2:3]
	s_mul_i32 s21, s21, s19
	s_sub_i32 s4, s18, s21
	s_lshl_b32 s4, s4, 6
	v_mov_b32_e32 v1, v2
	s_ashr_i32 s5, s4, 31
	v_lshl_add_u64 v[0:1], v[0:1], 2, s[34:35]
	s_lshl_b64 s[40:41], s[4:5], 2
	v_mov_b32_e32 v129, 0
	v_lshl_add_u64 v[0:1], v[0:1], 0, s[40:41]
	v_lshlrev_b32_e32 v128, 2, v66
	v_add_u32_e32 v8, 16, v40
	v_add_u32_e32 v16, 32, v40
	v_lshl_add_u64 v[24:25], v[0:1], 0, v[128:129]
	v_mad_u64_u32 v[0:1], s[4:5], v40, s28, 0
	v_ashrrev_i32_e32 v11, 31, v8
	v_mad_u64_u32 v[8:9], s[4:5], v8, s28, 0
	v_ashrrev_i32_e32 v19, 31, v16
	v_mad_u64_u32 v[16:17], s[4:5], v16, s28, 0
	v_ashrrev_i32_e32 v3, 31, v40
	v_mov_b32_e32 v2, v1
	v_mov_b32_e32 v10, v9
	v_mov_b32_e32 v18, v17
	v_mad_u64_u32 v[2:3], s[4:5], v3, s28, v[2:3]
	v_mad_u64_u32 v[10:11], s[4:5], v11, s28, v[10:11]
	v_mad_u64_u32 v[18:19], s[4:5], v19, s28, v[18:19]
	v_mov_b32_e32 v1, v2
	v_mov_b32_e32 v9, v10
	v_mov_b32_e32 v17, v18
	v_lshl_add_u64 v[0:1], v[0:1], 2, s[34:35]
	v_lshl_add_u64 v[8:9], v[8:9], 2, s[34:35]
	v_lshl_add_u64 v[16:17], v[16:17], 2, s[34:35]
	v_lshl_add_u64 v[0:1], v[0:1], 0, s[40:41]
	v_lshl_add_u64 v[8:9], v[8:9], 0, s[40:41]
	v_lshl_add_u64 v[16:17], v[16:17], 0, s[40:41]
	v_lshl_add_u64 v[32:33], v[0:1], 0, v[128:129]
	v_add_u32_e32 v0, 8, v40
	v_lshl_add_u64 v[28:29], v[8:9], 0, v[128:129]
	v_add_u32_e32 v8, 24, v40
	v_lshl_add_u64 v[36:37], v[16:17], 0, v[128:129]
	v_add_u32_e32 v16, 40, v40
	v_add_u32_e32 v40, 48, v40
	v_ashrrev_i32_e32 v43, 31, v40
	v_mad_u64_u32 v[40:41], s[4:5], v40, s28, 0
	v_ashrrev_i32_e32 v3, 31, v0
	v_mad_u64_u32 v[0:1], s[4:5], v0, s28, 0
	v_ashrrev_i32_e32 v11, 31, v8
	v_mad_u64_u32 v[8:9], s[4:5], v8, s28, 0
	v_ashrrev_i32_e32 v19, 31, v16
	v_mad_u64_u32 v[16:17], s[4:5], v16, s28, 0
	v_mov_b32_e32 v42, v41
	v_mov_b32_e32 v2, v1
	v_mov_b32_e32 v10, v9
	v_mov_b32_e32 v18, v17
	v_mad_u64_u32 v[42:43], s[4:5], v43, s28, v[42:43]
	v_mad_u64_u32 v[2:3], s[4:5], v3, s28, v[2:3]
	v_mad_u64_u32 v[10:11], s[4:5], v11, s28, v[10:11]
	v_mad_u64_u32 v[18:19], s[4:5], v19, s28, v[18:19]
	v_mov_b32_e32 v41, v42
	s_mov_b32 s29, 0
	v_mov_b32_e32 v1, v2
	v_mov_b32_e32 v9, v10
	v_mov_b32_e32 v17, v18
	v_lshl_add_u64 v[40:41], v[40:41], 2, s[34:35]
	s_lshl_b64 s[36:37], s[28:29], 2
	v_lshl_add_u64 v[0:1], v[0:1], 2, s[34:35]
	v_lshl_add_u64 v[8:9], v[8:9], 2, s[34:35]
	v_lshl_add_u64 v[16:17], v[16:17], 2, s[34:35]
	v_lshl_add_u64 v[40:41], v[40:41], 0, s[40:41]
	v_lshl_add_u64 v[26:27], v[24:25], 0, s[36:37]
	v_lshl_add_u64 v[0:1], v[0:1], 0, s[40:41]
	v_lshl_add_u64 v[8:9], v[8:9], 0, s[40:41]
	v_lshl_add_u64 v[16:17], v[16:17], 0, s[40:41]
	v_lshl_add_u64 v[40:41], v[40:41], 0, v[128:129]
	v_lshl_add_u64 v[34:35], v[0:1], 0, v[128:129]
	global_load_dwordx4 v[0:3], v[32:33], off nt
	global_load_dwordx4 v[4:7], v[34:35], off nt
	v_lshl_add_u64 v[30:31], v[8:9], 0, v[128:129]
	global_load_dwordx4 v[8:11], v[28:29], off nt
	global_load_dwordx4 v[12:15], v[30:31], off nt
	v_lshl_add_u64 v[38:39], v[16:17], 0, v[128:129]
	global_load_dwordx4 v[16:19], v[36:37], off nt
	global_load_dwordx4 v[20:23], v[38:39], off nt
	global_load_dwordx4 v[48:51], v[26:27], off nt
	global_load_dwordx4 v[52:55], v[24:25], off nt
	v_lshl_add_u64 v[24:25], v[40:41], 0, s[36:37]
	global_load_dwordx4 v[44:47], v[40:41], off nt
	global_load_dwordx4 v[56:59], v[24:25], off nt
	v_lshl_add_u64 v[24:25], v[38:39], 0, s[36:37]
	v_lshl_add_u64 v[26:27], v[36:37], 0, s[36:37]
	global_load_dwordx4 v[60:63], v[24:25], off nt
	global_load_dwordx4 v[36:39], v[26:27], off nt
	v_lshl_add_u64 v[24:25], v[30:31], 0, s[36:37]
	v_lshl_add_u64 v[26:27], v[28:29], 0, s[36:37]
	global_load_dwordx4 v[40:43], v[24:25], off nt
	global_load_dwordx4 v[28:31], v[26:27], off nt
	v_lshl_add_u64 v[24:25], v[34:35], 0, s[36:37]
	v_lshl_add_u64 v[26:27], v[32:33], 0, s[36:37]
	global_load_dwordx4 v[32:35], v[24:25], off nt
	s_nop 0
	global_load_dwordx4 v[24:27], v[26:27], off nt
	s_waitcnt lgkmcnt(0)
	s_add_u32 s19, s38, 0x26000000
	s_addc_u32 s24, s39, 0
	s_add_u32 s25, s38, 0x6000000
	s_addc_u32 s50, s39, 0
	s_add_u32 s34, s38, 0x5800000
	s_addc_u32 s35, s39, 0
	s_add_u32 s36, s38, 0x4800000
	s_addc_u32 s37, s39, 0
	v_ashrrev_i32_e32 v65, 4, v64
	s_movk_i32 s4, 0x104
	v_and_b32_e32 v64, 7, v64
	s_add_u32 s38, s38, 0x800000
	v_add_u32_e32 v67, s20, v128
	v_mul_lo_u32 v65, v65, s4
	v_mul_u32_u24_e32 v68, 0x410, v64
	v_lshlrev_b32_e32 v64, 3, v64
	v_lshlrev_b32_e32 v69, 2, v132
	s_addc_u32 s39, s39, 0
	v_add3_u32 v134, s20, v68, v69
	v_add_u32_e32 v135, 8, v132
	v_add_u32_e32 v136, 16, v132
	v_add_u32_e32 v137, 24, v132
	v_add_u32_e32 v138, 32, v132
	v_add_u32_e32 v139, 40, v132
	v_add_u32_e32 v140, 48, v132
	v_add_u32_e32 v141, 56, v132
	v_lshlrev_b32_e32 v128, 2, v66
	v_lshlrev_b32_e32 v130, 1, v64
	v_add_u32_e32 v142, v67, v65
	s_mov_b32 s4, s28
	s_mov_b32 s98, 0
	s_branch .LBB0_2248

; #define GAS __attribute__((address_space(1)))
; __device__ __forceinline__ void conv_load(const ConvSrc& c, int lane, f32x4 (&ra)[8], f32x4 (&rb)[8]) {
;     const int nblk = c.N >> 6, kb = c.kfast ? (c.item & 31) : c.item / nblk, nb = c.kfast ? (c.item >> 5) : c.item - kb * nblk, k0 = kb * 64, n0 = nb * 64;
;     const int n4 = (lane & 15) * 4, kq = lane >> 4;
; #pragma unroll
;     for (int i = 0; i < 8; ++i) { const int kp2 = 4 * i + kq; const float* p = c.W + (size_t)(k0 + 2 * kp2) * c.N + n0 + n4; ra[i] = __builtin_nontemporal_load((const GAS f32x4*)p); rb[i] = __builtin_nontemporal_load((const GAS f32x4*)(p + c.N)); }
; }
; __device__ __forceinline__ void conv_run(KP kp, unsigned char* ws, LAS unsigned* P, int lane, int first, int it_hi, int step) {
;     ...
;         c1 = conv_decode(kp, ws, min(it + step, lastv)); conv_load(c1, lane, a1, b1);
.LBB0_2267:
	s_lshr_b32 s42, s28, 6
	v_cvt_f32_u32_e32 v64, s42
	s_sub_i32 s47, 0, s42
	s_abs_i32 s43, s46
	s_ashr_i32 s21, s46, 31
	v_rcp_iflag_f32_e32 v64, v64
	s_nop 0
	v_mul_f32_e32 v64, 0x4f7ffffe, v64
	v_cvt_u32_f32_e32 v64, v64
	s_nop 0
	v_readfirstlane_b32 s48, v64
	s_mul_i32 s47, s47, s48
	s_mul_hi_u32 s47, s48, s47
	s_add_i32 s48, s48, s47
	s_mul_hi_u32 s47, s43, s48
	s_mul_i32 s48, s47, s42
	s_sub_i32 s43, s43, s48
	s_add_i32 s49, s47, 1
	s_sub_i32 s48, s43, s42
	s_cmp_ge_u32 s43, s42
	s_cselect_b32 s47, s49, s47
	s_cselect_b32 s43, s48, s43
	s_add_i32 s48, s47, 1
	s_cmp_ge_u32 s43, s42
	s_cselect_b32 s43, s48, s47
	s_xor_b32 s43, s43, s21
	s_sub_i32 s21, s43, s21
	s_mul_i32 s42, s21, s42
	v_lshl_add_u32 v120, s21, 6, v133
	s_sub_i32 s53, s46, s42
	v_mad_u64_u32 v[64:65], s[42:43], v120, s28, 0
	v_ashrrev_i32_e32 v67, 31, v120
	v_mov_b32_e32 v66, v65
	s_lshl_b32 s42, s53, 6
	v_mad_u64_u32 v[66:67], s[46:47], v67, s28, v[66:67]
	s_ashr_i32 s43, s42, 31
	v_mov_b32_e32 v65, v66
	s_waitcnt lgkmcnt(0)
	v_lshl_add_u64 v[64:65], v[64:65], 2, s[44:45]
	s_lshl_b64 s[46:47], s[42:43], 2
	v_lshl_add_u64 v[64:65], v[64:65], 0, s[46:47]
	v_lshl_add_u64 v[64:65], v[64:65], 0, v[128:129]
	s_lshl_b64 s[48:49], s[28:29], 2
	v_lshl_add_u64 v[68:69], v[64:65], 0, s[48:49]
	global_load_dwordx4 v[64:67], v[64:65], off nt
	s_nop 0
	global_load_dwordx4 v[92:95], v[68:69], off nt
	v_add_u32_e32 v68, 8, v120
	v_ashrrev_i32_e32 v71, 31, v68
	v_mad_u64_u32 v[68:69], s[54:55], v68, s28, 0
	v_mov_b32_e32 v70, v69
	v_mad_u64_u32 v[70:71], s[54:55], v71, s28, v[70:71]
	v_mov_b32_e32 v69, v70
	v_lshl_add_u64 v[68:69], v[68:69], 2, s[44:45]
	v_lshl_add_u64 v[68:69], v[68:69], 0, s[46:47]
	v_lshl_add_u64 v[68:69], v[68:69], 0, v[128:129]
	v_lshl_add_u64 v[72:73], v[68:69], 0, s[48:49]
	global_load_dwordx4 v[68:71], v[68:69], off nt
	s_nop 0
	global_load_dwordx4 v[96:99], v[72:73], off nt
	v_add_u32_e32 v72, 16, v120
	v_ashrrev_i32_e32 v75, 31, v72
	v_mad_u64_u32 v[72:73], s[54:55], v72, s28, 0
	v_mov_b32_e32 v74, v73
	v_mad_u64_u32 v[74:75], s[54:55], v75, s28, v[74:75]
	v_mov_b32_e32 v73, v74
	v_lshl_add_u64 v[72:73], v[72:73], 2, s[44:45]
	v_lshl_add_u64 v[72:73], v[72:73], 0, s[46:47]
	v_lshl_add_u64 v[72:73], v[72:73], 0, v[128:129]
	v_lshl_add_u64 v[76:77], v[72:73], 0, s[48:49]
	global_load_dwordx4 v[72:75], v[72:73], off nt
	s_nop 0
	global_load_dwordx4 v[100:103], v[76:77], off nt
	v_add_u32_e32 v76, 24, v120
	v_ashrrev_i32_e32 v79, 31, v76
	v_mad_u64_u32 v[76:77], s[54:55], v76, s28, 0
	v_mov_b32_e32 v78, v77
	v_mad_u64_u32 v[78:79], s[54:55], v79, s28, v[78:79]
	v_mov_b32_e32 v77, v78
	v_lshl_add_u64 v[76:77], v[76:77], 2, s[44:45]
	v_lshl_add_u64 v[76:77], v[76:77], 0, s[46:47]
	v_lshl_add_u64 v[76:77], v[76:77], 0, v[128:129]
	v_lshl_add_u64 v[80:81], v[76:77], 0, s[48:49]
	global_load_dwordx4 v[76:79], v[76:77], off nt
	s_nop 0
	global_load_dwordx4 v[104:107], v[80:81], off nt
	v_add_u32_e32 v80, 32, v120
	v_ashrrev_i32_e32 v83, 31, v80
	v_mad_u64_u32 v[80:81], s[54:55], v80, s28, 0
	v_mov_b32_e32 v82, v81
	v_mad_u64_u32 v[82:83], s[54:55], v83, s28, v[82:83]
	v_mov_b32_e32 v81, v82
	v_lshl_add_u64 v[80:81], v[80:81], 2, s[44:45]
	v_lshl_add_u64 v[80:81], v[80:81], 0, s[46:47]
	v_lshl_add_u64 v[80:81], v[80:81], 0, v[128:129]
	v_lshl_add_u64 v[84:85], v[80:81], 0, s[48:49]
	global_load_dwordx4 v[80:83], v[80:81], off nt
	s_nop 0
	global_load_dwordx4 v[108:111], v[84:85], off nt
	v_add_u32_e32 v84, 40, v120
	v_ashrrev_i32_e32 v87, 31, v84
	v_mad_u64_u32 v[84:85], s[54:55], v84, s28, 0
	v_mov_b32_e32 v86, v85
	v_mad_u64_u32 v[86:87], s[54:55], v87, s28, v[86:87]
	v_mov_b32_e32 v85, v86
	v_lshl_add_u64 v[84:85], v[84:85], 2, s[44:45]
	v_lshl_add_u64 v[84:85], v[84:85], 0, s[46:47]
	v_lshl_add_u64 v[84:85], v[84:85], 0, v[128:129]
	v_lshl_add_u64 v[88:89], v[84:85], 0, s[48:49]
	global_load_dwordx4 v[84:87], v[84:85], off nt
	s_nop 0
	global_load_dwordx4 v[112:115], v[88:89], off nt
	v_add_u32_e32 v88, 48, v120
	v_add_u32_e32 v120, 56, v120
	v_ashrrev_i32_e32 v91, 31, v88
	v_mad_u64_u32 v[88:89], s[54:55], v88, s28, 0
	v_ashrrev_i32_e32 v123, 31, v120
	v_mad_u64_u32 v[120:121], s[54:55], v120, s28, 0
	v_mov_b32_e32 v90, v89
	v_mov_b32_e32 v122, v121
	v_mad_u64_u32 v[90:91], s[54:55], v91, s28, v[90:91]
	v_mad_u64_u32 v[122:123], s[54:55], v123, s28, v[122:123]
	v_mov_b32_e32 v89, v90
	v_mov_b32_e32 v121, v122
	s_lshr_b32 s4, s4, 6
	v_lshl_add_u64 v[88:89], v[88:89], 2, s[44:45]
	v_cvt_f32_u32_e32 v122, s4
	v_lshl_add_u64 v[120:121], v[120:121], 2, s[44:45]
	v_lshl_add_u64 v[88:89], v[88:89], 0, s[46:47]
	v_lshl_add_u64 v[120:121], v[120:121], 0, s[46:47]
	v_lshl_add_u64 v[88:89], v[88:89], 0, v[128:129]
	v_lshl_add_u64 v[120:121], v[120:121], 0, v[128:129]
	v_lshl_add_u64 v[116:117], v[88:89], 0, s[48:49]
	v_lshl_add_u64 v[124:125], v[120:121], 0, s[48:49]
	global_load_dwordx4 v[88:91], v[88:89], off nt
	s_nop 0
	global_load_dwordx4 v[116:119], v[116:117], off nt
	v_rcp_iflag_f32_e32 v131, v122
	global_load_dwordx4 v[120:123], v[120:121], off nt
	s_nop 0
	global_load_dwordx4 v[124:127], v[124:125], off nt
	s_cmp_eq_u32 s98, 0
	s_cbranch_scc1 .Lcw_first_3
	s_waitcnt vmcnt(24)
	s_branch .Lcw_done_3

; #define GAS __attribute__((address_space(1)))
; #define LAS __attribute__((address_space(3)))
; __device__ __forceinline__ ConvSrc conv_decode(KP kp, unsigned char* ws, int it) {
;     constexpr int I_IN = 32 * 256, I_SQ = 32 * 32, I_UP = 32 * 64, I_DN = 32 * 32;
;     ConvSrc c; int r = it; c.ldk = 2048; c.kfast = 0; c.tiled = 32; c.ktoff = 0;
;     if (r < I_IN) { c.W = (const float*)KIN(6); c.WT = (bf16*)(ws + WS_WIN); c.N = 16384; c.item = r; return c; } r -= I_IN;
;     if (r < I_SQ) { c.W = (const float*)KIN(13); c.WT = (bf16*)(ws + WS_WAO); c.N = 2048; c.item = r; c.ldk = 4096; c.tiled = 64; return c; } r -= I_SQ;
;     if (r < I_SQ) { c.W = (const float*)KIN(14); c.WT = (bf16*)(ws + WS_WAO); c.N = 2048; c.item = r; c.ldk = 4096; c.tiled = 64; c.ktoff = 32; return c; } r -= I_SQ;
;     if (r < I_SQ) { c.W = (const float*)KIN(15); c.WT = (bf16*)(ws + WS_WO); c.N = 2048; c.item = r; return c; } r -= I_SQ;
;     if (r < NE * I_UP) { const int e = r / I_UP; c.W = (const float*)KIN(19) + (size_t)e * 2048 * 4096; c.WT = (bf16*)(ws + WS_WUP) + (size_t)e * 4096 * 2048; c.N = 4096; c.item = r - e * I_UP; return c; } r -= NE * I_UP;
; __device__ __forceinline__ void conv_emit(const ConvSrc& c, int lane, LAS unsigned* P, const f32x4 (&ra)[8], const f32x4 (&rb)[8]) {
;     const int nblk = c.N >> 6, kb = c.kfast ? (c.item & 31) : c.item / nblk, nb = c.kfast ? (c.item >> 5) : c.item - kb * nblk, k0 = kb * 64, n0 = nb * 64;
;     const int n4 = (lane & 15) * 4, kq = lane >> 4;
; #pragma unroll
;     for (int i = 0; i < 8; ++i) { const int kp2 = 4 * i + kq; LAS unsigned* d = P + kp2 * 65 + n4;
;         d[0] = pg8::cvt_pk_bf16(ra[i].x, rb[i].x); d[1] = pg8::cvt_pk_bf16(ra[i].y, rb[i].y); d[2] = pg8::cvt_pk_bf16(ra[i].z, rb[i].z); d[3] = pg8::cvt_pk_bf16(ra[i].w, rb[i].w); }
;     LDS_WAIT(); asm volatile("" ::: "memory");
;     const int cc = lane & 7;
; #pragma unroll
;     for (int jj = 0; jj < 8; ++jj) { const int n = (lane >> 3) + 8 * jj; const LAS unsigned* sp = P + (4 * cc) * 65 + n;
;         v4u o; o.x = sp[0]; o.y = sp[65]; o.z = sp[130]; o.w = sp[195];
;         bf16* dst = c.tiled ? c.WT + (size_t)((nb >> 2) * c.tiled + c.ktoff + kb) * 16384 + ((nb & 3) * 64 + n) * 64 + 8 * cc : c.WT + (size_t)(n0 + n) * c.ldk + k0 + 8 * cc;
;         __builtin_nontemporal_store(o, (GAS v4u*)dst); }
;     LDS_WAIT(); asm volatile("" ::: "memory");
.Lcw_done_3:
	v_cvt_pk_bf16_f32 v0, v0, v24
	ds_write_b32 v142, v0
	v_cvt_pk_bf16_f32 v0, v1, v25
	ds_write_b32 v142, v0 offset:4
	v_cvt_pk_bf16_f32 v0, v2, v26
	ds_write_b32 v142, v0 offset:8
	v_cvt_pk_bf16_f32 v0, v3, v27
	ds_write_b32 v142, v0 offset:12
	v_cvt_pk_bf16_f32 v0, v4, v32
	ds_write_b32 v142, v0 offset:1040
	v_cvt_pk_bf16_f32 v0, v5, v33
	ds_write_b32 v142, v0 offset:1044
	v_cvt_pk_bf16_f32 v0, v6, v34
	ds_write_b32 v142, v0 offset:1048
	v_cvt_pk_bf16_f32 v0, v7, v35
	ds_write_b32 v142, v0 offset:1052
	v_cvt_pk_bf16_f32 v0, v8, v28
	v_mul_f32_e32 v131, 0x4f7ffffe, v131
	ds_write_b32 v142, v0 offset:2080
	v_cvt_pk_bf16_f32 v0, v9, v29
	v_cvt_u32_f32_e32 v131, v131
	ds_write_b32 v142, v0 offset:2084
	v_cvt_pk_bf16_f32 v0, v10, v30
	ds_write_b32 v142, v0 offset:2088
	v_cvt_pk_bf16_f32 v0, v11, v31
	ds_write_b32 v142, v0 offset:2092
	v_cvt_pk_bf16_f32 v0, v12, v40
	ds_write_b32 v142, v0 offset:3120
	v_cvt_pk_bf16_f32 v0, v13, v41
	s_sub_i32 s44, 0, s4
	v_readfirstlane_b32 s45, v131
	ds_write_b32 v142, v0 offset:3124
	v_cvt_pk_bf16_f32 v0, v14, v42
	s_mul_i32 s44, s44, s45
	ds_write_b32 v142, v0 offset:3128
	v_cvt_pk_bf16_f32 v0, v15, v43
	s_mul_hi_u32 s44, s45, s44
	ds_write_b32 v142, v0 offset:3132
	v_cvt_pk_bf16_f32 v0, v16, v36
	s_abs_i32 s43, s18
	s_add_i32 s45, s45, s44
	ds_write_b32 v142, v0 offset:4160
	v_cvt_pk_bf16_f32 v0, v17, v37
	s_mul_hi_u32 s44, s43, s45
	ds_write_b32 v142, v0 offset:4164
	v_cvt_pk_bf16_f32 v0, v18, v38
	s_mul_i32 s45, s44, s4
	ds_write_b32 v142, v0 offset:4168
	v_cvt_pk_bf16_f32 v0, v19, v39
	s_sub_i32 s43, s43, s45
	ds_write_b32 v142, v0 offset:4172
	v_cvt_pk_bf16_f32 v0, v20, v60
	s_ashr_i32 s28, s18, 31
	s_add_i32 s45, s44, 1
	s_sub_i32 s46, s43, s4
	ds_write_b32 v142, v0 offset:5200
	v_cvt_pk_bf16_f32 v0, v21, v61
	s_cmp_ge_u32 s43, s4
	ds_write_b32 v142, v0 offset:5204
	v_cvt_pk_bf16_f32 v0, v22, v62
	s_cselect_b32 s44, s45, s44
	ds_write_b32 v142, v0 offset:5208
	v_cvt_pk_bf16_f32 v0, v23, v63
	s_cselect_b32 s43, s46, s43
	s_add_i32 s45, s44, 1
	ds_write_b32 v142, v0 offset:5212
	v_cvt_pk_bf16_f32 v0, v44, v56
	s_cmp_ge_u32 s43, s4
	ds_write_b32 v142, v0 offset:6240
	v_cvt_pk_bf16_f32 v0, v45, v57
	s_cselect_b32 s43, s45, s44
	ds_write_b32 v142, v0 offset:6244
	v_cvt_pk_bf16_f32 v0, v46, v58
	s_xor_b32 s43, s43, s28
	ds_write_b32 v142, v0 offset:6248
	v_cvt_pk_bf16_f32 v0, v47, v59
	s_sub_i32 s28, s43, s28
	ds_write_b32 v142, v0 offset:6252
	v_cvt_pk_bf16_f32 v0, v52, v48
	s_mul_i32 s4, s28, s4
	ds_write_b32 v142, v0 offset:7280
	v_cvt_pk_bf16_f32 v0, v53, v49
	s_sub_i32 s4, s18, s4
	ds_write_b32 v142, v0 offset:7284
	v_cvt_pk_bf16_f32 v0, v54, v50
	ds_write_b32 v142, v0 offset:7288
	v_cvt_pk_bf16_f32 v0, v55, v51
	ds_write_b32 v142, v0 offset:7292
	s_lshl_b32 s18, s4, 6
	s_ashr_i32 s4, s4, 2
	s_waitcnt lgkmcnt(0)
	s_mul_i32 s4, s4, s52
	s_add_i32 s28, s28, s51
	s_add_i32 s44, s28, s4
	ds_read2_b32 v[8:9], v134 offset1:8
	ds_read2_b32 v[0:1], v134 offset0:65 offset1:73
	ds_read2_b32 v[10:11], v134 offset0:130 offset1:138
	ds_read2_b32 v[2:3], v134 offset0:195 offset1:203
	s_ashr_i32 s45, s44, 31
	s_and_b32 s18, s18, 0xc0
	s_lshl_b64 s[44:45], s[44:45], 15
	s_add_u32 s30, s30, s44
	v_add_lshl_u32 v12, s18, v132, 6
	s_addc_u32 s31, s31, s45
	v_ashrrev_i32_e32 v13, 31, v12
	v_lshl_add_u64 v[12:13], v[12:13], 1, s[30:31]
	v_mov_b32_e32 v131, v129
	s_waitcnt lgkmcnt(3)
	v_mov_b32_e32 v4, v8
	s_waitcnt lgkmcnt(2)
	v_mov_b32_e32 v5, v0
	s_waitcnt lgkmcnt(1)
	v_mov_b32_e32 v6, v10
	s_waitcnt lgkmcnt(0)
	v_mov_b32_e32 v7, v2
	v_lshl_add_u64 v[12:13], v[12:13], 0, v[130:131]
	global_store_dwordx4 v[12:13], v[4:7], off nt
	v_mov_b32_e32 v0, v9
	v_mov_b32_e32 v2, v11
	v_add_lshl_u32 v4, s18, v135, 6
	v_ashrrev_i32_e32 v5, 31, v4
	v_lshl_add_u64 v[4:5], v[4:5], 1, s[30:31]
	v_lshl_add_u64 v[8:9], v[4:5], 0, v[130:131]
	ds_read2_b32 v[10:11], v134 offset0:16 offset1:24
	ds_read2_b32 v[4:5], v134 offset0:81 offset1:89
	ds_read2_b32 v[12:13], v134 offset0:146 offset1:154
	ds_read2_b32 v[6:7], v134 offset0:211 offset1:219
	global_store_dwordx4 v[8:9], v[0:3], off nt
	v_add_lshl_u32 v8, s18, v136, 6
	v_ashrrev_i32_e32 v9, 31, v8
	v_lshl_add_u64 v[8:9], v[8:9], 1, s[30:31]
	s_waitcnt lgkmcnt(3)
	v_mov_b32_e32 v0, v10
	s_waitcnt lgkmcnt(2)
	v_mov_b32_e32 v1, v4
	s_waitcnt lgkmcnt(1)
	v_mov_b32_e32 v2, v12
	s_waitcnt lgkmcnt(0)
	v_mov_b32_e32 v3, v6
	v_lshl_add_u64 v[8:9], v[8:9], 0, v[130:131]
	global_store_dwordx4 v[8:9], v[0:3], off nt
	v_mov_b32_e32 v4, v11
	v_mov_b32_e32 v6, v13
	v_add_lshl_u32 v0, s18, v137, 6
	v_ashrrev_i32_e32 v1, 31, v0
	v_lshl_add_u64 v[0:1], v[0:1], 1, s[30:31]
	v_lshl_add_u64 v[8:9], v[0:1], 0, v[130:131]
	ds_read2_b32 v[10:11], v134 offset0:32 offset1:40
	ds_read2_b32 v[0:1], v134 offset0:97 offset1:105
	ds_read2_b32 v[12:13], v134 offset0:162 offset1:170
	ds_read2_b32 v[2:3], v134 offset0:227 offset1:235
	global_store_dwordx4 v[8:9], v[4:7], off nt
	v_add_lshl_u32 v8, s18, v138, 6
	v_ashrrev_i32_e32 v9, 31, v8
	v_lshl_add_u64 v[8:9], v[8:9], 1, s[30:31]
	s_waitcnt lgkmcnt(3)
	v_mov_b32_e32 v4, v10
	s_waitcnt lgkmcnt(2)
	v_mov_b32_e32 v5, v0
	s_waitcnt lgkmcnt(1)
	v_mov_b32_e32 v6, v12
	s_waitcnt lgkmcnt(0)
	v_mov_b32_e32 v7, v2
	v_lshl_add_u64 v[8:9], v[8:9], 0, v[130:131]
	global_store_dwordx4 v[8:9], v[4:7], off nt
	v_mov_b32_e32 v0, v11
	v_mov_b32_e32 v2, v13
	v_add_lshl_u32 v4, s18, v139, 6
	v_ashrrev_i32_e32 v5, 31, v4
	v_lshl_add_u64 v[4:5], v[4:5], 1, s[30:31]
	v_lshl_add_u64 v[8:9], v[4:5], 0, v[130:131]
	ds_read2_b32 v[10:11], v134 offset0:48 offset1:56
	ds_read2_b32 v[4:5], v134 offset0:113 offset1:121
	ds_read2_b32 v[12:13], v134 offset0:178 offset1:186
	ds_read2_b32 v[6:7], v134 offset0:243 offset1:251
	global_store_dwordx4 v[8:9], v[0:3], off nt
	v_add_lshl_u32 v8, s18, v140, 6
	v_ashrrev_i32_e32 v9, 31, v8
	v_lshl_add_u64 v[8:9], v[8:9], 1, s[30:31]
	s_waitcnt lgkmcnt(3)
	v_mov_b32_e32 v0, v10
	s_waitcnt lgkmcnt(2)
	v_mov_b32_e32 v1, v4
	s_waitcnt lgkmcnt(1)
	v_mov_b32_e32 v2, v12
	s_waitcnt lgkmcnt(0)
	v_mov_b32_e32 v3, v6
	v_lshl_add_u64 v[8:9], v[8:9], 0, v[130:131]
	global_store_dwordx4 v[8:9], v[0:3], off nt
	v_mov_b32_e32 v4, v11
	v_mov_b32_e32 v6, v13
	v_add_lshl_u32 v0, s18, v141, 6
	v_ashrrev_i32_e32 v1, 31, v0
	v_lshl_add_u64 v[0:1], v[0:1], 1, s[30:31]
	v_lshl_add_u64 v[0:1], v[0:1], 0, v[130:131]
	global_store_dwordx4 v[0:1], v[4:7], off nt
	s_waitcnt lgkmcnt(0)
	s_add_i32 s22, s22, 16
	s_min_i32 s4, s22, s23
	s_cmpk_gt_i32 s4, 0x1fff
	s_mov_b64 s[46:47], -1
	s_cbranch_scc0 .LBB0_2284
	s_cmpk_gt_u32 s4, 0x23ff
	s_cbranch_scc0 .LBB0_2281
	s_cmpk_gt_u32 s4, 0x27ff
	s_cbranch_scc0 .LBB0_2279
	s_cmpk_gt_u32 s4, 0x2bff
	s_cbranch_scc0 .LBB0_2276
	s_cmp_gt_u32 s4, 0x12bff
	s_cbranch_scc0 .LBB0_2273
	s_load_dwordx2 s[30:31], s[2:3], 0xa8
	s_add_i32 s18, s4, 0xfffed400
	s_lshr_b32 s28, s18, 10
	s_lshl_b64 s[44:45], s[28:29], 24
	s_mov_b64 s[46:47], 0
	s_waitcnt lgkmcnt(0)
	s_add_u32 s44, s30, s44
	s_addc_u32 s45, s31, s45
	s_lshl_b64 s[30:31], s[28:29], 23
	s_add_u32 s30, s19, s30
	s_addc_u32 s31, s24, s31
	s_and_b32 s18, s4, 0x3ff

; #define LAS __attribute__((address_space(3)))
; __global__ void __launch_bounds__(NWAVES * 64, 2) mk_fwd(Args args) {
;     extern __shared__ __attribute__((aligned(16))) unsigned char lds_raw[];
;     LAS unsigned char* lds = (LAS unsigned char*)lds_raw;
;     volatile LAS unsigned* MISC = (volatile LAS unsigned*)(lds + MISC_OFF);
;     const int wave = __builtin_amdgcn_readfirstlane(threadIdx.x >> 6);
	.amdhsa_kernel _Z6mk_fwd4Args
		.amdhsa_group_segment_fixed_size 0
		.amdhsa_private_segment_fixed_size 0
		.amdhsa_kernarg_size 480
		.amdhsa_user_sgpr_count 2
		.amdhsa_user_sgpr_dispatch_ptr 0
		.amdhsa_user_sgpr_queue_ptr 0
		.amdhsa_user_sgpr_kernarg_segment_ptr 1
		.amdhsa_user_sgpr_dispatch_id 0
		.amdhsa_user_sgpr_kernarg_preload_length 0
		.amdhsa_user_sgpr_kernarg_preload_offset 0
		.amdhsa_user_sgpr_private_segment_size 0
		.amdhsa_uses_dynamic_stack 0
		.amdhsa_enable_private_segment 0
		.amdhsa_system_sgpr_workgroup_id_x 1
		.amdhsa_system_sgpr_workgroup_id_y 0
		.amdhsa_system_sgpr_workgroup_id_z 0
		.amdhsa_system_sgpr_workgroup_info 0
		.amdhsa_system_vgpr_workitem_id 0
		.amdhsa_next_free_vgpr 247
		.amdhsa_next_free_sgpr 99
		.amdhsa_accum_offset 248
		.amdhsa_reserve_vcc 1
		.amdhsa_float_round_mode_32 0
		.amdhsa_float_round_mode_16_64 0
		.amdhsa_float_denorm_mode_32 3
		.amdhsa_float_denorm_mode_16_64 3
		.amdhsa_dx10_clamp 1
		.amdhsa_ieee_mode 1
		.amdhsa_fp16_overflow 0
		.amdhsa_tg_split 0
		.amdhsa_exception_fp_ieee_invalid_op 0
		.amdhsa_exception_fp_denorm_src 0
		.amdhsa_exception_fp_ieee_div_zero 0
		.amdhsa_exception_fp_ieee_overflow 0
		.amdhsa_exception_fp_ieee_underflow 0
		.amdhsa_exception_fp_ieee_inexact 0
		.amdhsa_exception_int_div_zero 0
	.end_amdhsa_kernel

; #define LAS __attribute__((address_space(3)))
; __global__ void __launch_bounds__(NWAVES * 64, 2) mk_fwd(Args args) {
;     extern __shared__ __attribute__((aligned(16))) unsigned char lds_raw[];
;     LAS unsigned char* lds = (LAS unsigned char*)lds_raw;
;     volatile LAS unsigned* MISC = (volatile LAS unsigned*)(lds + MISC_OFF);
;     const int wave = __builtin_amdgcn_readfirstlane(threadIdx.x >> 6);
amdhsa.kernels:
  - .agpr_count:     0
    .args:
      - .offset:         0
        .size:           224
        .value_kind:     by_value
      - .offset:         224
        .size:           4
        .value_kind:     hidden_block_count_x
      - .offset:         228
        .size:           4
        .value_kind:     hidden_block_count_y
      - .offset:         232
        .size:           4
        .value_kind:     hidden_block_count_z
      - .offset:         236
        .size:           2
        .value_kind:     hidden_group_size_x
      - .offset:         238
        .size:           2
        .value_kind:     hidden_group_size_y
      - .offset:         240
        .size:           2
        .value_kind:     hidden_group_size_z
      - .offset:         242
        .size:           2
        .value_kind:     hidden_remainder_x
      - .offset:         244
        .size:           2
        .value_kind:     hidden_remainder_y
      - .offset:         246
        .size:           2
        .value_kind:     hidden_remainder_z
      - .offset:         264
        .size:           8
        .value_kind:     hidden_global_offset_x
      - .offset:         272
        .size:           8
        .value_kind:     hidden_global_offset_y
      - .offset:         280
        .size:           8
        .value_kind:     hidden_global_offset_z
      - .offset:         288
        .size:           2
        .value_kind:     hidden_grid_dims
      - .offset:         344
        .size:           4
        .value_kind:     hidden_dynamic_lds_size
    .group_segment_fixed_size: 0
    .kernarg_segment_align: 8
    .kernarg_segment_size: 480
    .language:       OpenCL C
    .language_version:
      - 2
      - 0
    .max_flat_workgroup_size: 512
    .name:           _Z6mk_fwd4Args
    .private_segment_fixed_size: 0
    .sgpr_count:     105
    .sgpr_spill_count: 11
    .symbol:         _Z6mk_fwd4Args.kd
    .uniform_work_group_size: 1
    .uses_dynamic_stack: false
    .vgpr_count:     247
    .vgpr_spill_count: 0
    .wavefront_size: 64
